# stack + phase 0: 6-instruction integer bf16 round-to-nearest-even packs replaced by v_cvt_pk_bf16_f32 (232 sites)
# speedup vs baseline: 1.0164x; 1.0026x over previous
; #define LAS __attribute__((address_space(3)))
; __device__ __forceinline__ unsigned pk2(float lo, float hi) { return f2bf(lo) | (f2bf(hi) << 16); }
; template <int MAPK>
; __device__ __forceinline__ void transpose_item(const float* W, int ldw, int k0, int n0, int ncnt, bf16* WT, int ldd, int dcol0, int moff, LAS float* scr, int lane, const float* gk) {
;     ...
;     const int c = lane & 7;
; #pragma unroll
;     for (int j = 0; j < 4; ++j) { const int n = (lane >> 3) + 8 * j; const LAS float* s = scr + (8 * c) * 33 + n;
;         v4u o; o.x = pk2(s[0 * 33], s[1 * 33]); o.y = pk2(s[2 * 33], s[3 * 33]); o.z = pk2(s[4 * 33], s[5 * 33]); o.w = pk2(s[6 * 33], s[7 * 33]);
;         const int sn = n0 + n - moff;
;         int drow;
;         if (MAPK == MAP_LIN) drow = sn; else if (MAPK == MAP_GATE) drow = 32 * (sn >> 4) + (sn & 15); else drow = 32 * (sn >> 4) + 16 + (sn & 15);
;         if (n < ncnt) *(v4u*)(WT + (size_t)drow * ldd + dcol0 + k0 + 8 * c) = o; }
.LBB0_47:
	s_or_b64 exec, exec, s[26:27]
	s_waitcnt vmcnt(0)
	v_lshlrev_b32_e32 v91, 2, v35
	ds_bpermute_b32 v78, v91, v90
	ds_bpermute_b32 v76, v91, v90 offset:32
	ds_bpermute_b32 v74, v91, v90 offset:64
	ds_bpermute_b32 v72, v91, v90 offset:96
	ds_bpermute_b32 v70, v91, v90 offset:128
	ds_bpermute_b32 v68, v91, v90 offset:160
	ds_bpermute_b32 v66, v91, v90 offset:192
	ds_bpermute_b32 v64, v91, v90 offset:224
	s_waitcnt lgkmcnt(0)
	v_add_u32_e32 v0, v37, v67
	v_pk_mul_f32 v[2:3], v[78:79], v[2:3] op_sel_hi:[0,1]
	v_pk_mul_f32 v[4:5], v[78:79], v[4:5] op_sel_hi:[0,1]
	v_pk_mul_f32 v[6:7], v[76:77], v[6:7] op_sel_hi:[0,1]
	ds_write2_b32 v0, v2, v3 offset1:1
	ds_write2_b32 v0, v4, v5 offset0:2 offset1:3
	v_add_u32_e32 v2, 0x420, v0
	v_pk_mul_f32 v[8:9], v[76:77], v[8:9] op_sel_hi:[0,1]
	ds_write2_b32 v2, v6, v7 offset1:1
	v_add_u32_e32 v2, 0x428, v0
	v_pk_mul_f32 v[14:15], v[74:75], v[14:15] op_sel_hi:[0,1]
	ds_write2_b32 v2, v8, v9 offset1:1
	v_add_u32_e32 v2, 0x840, v0
	v_pk_mul_f32 v[16:17], v[74:75], v[16:17] op_sel_hi:[0,1]
	ds_write2_b32 v2, v14, v15 offset1:1
	v_add_u32_e32 v2, 0x848, v0
	v_pk_mul_f32 v[10:11], v[72:73], v[10:11] op_sel_hi:[0,1]
	ds_write2_b32 v2, v16, v17 offset1:1
	v_add_u32_e32 v2, 0xc60, v0
	v_pk_mul_f32 v[12:13], v[72:73], v[12:13] op_sel_hi:[0,1]
	ds_write2_b32 v2, v10, v11 offset1:1
	v_add_u32_e32 v2, 0xc68, v0
	v_pk_mul_f32 v[22:23], v[70:71], v[22:23] op_sel_hi:[0,1]
	ds_write2_b32 v2, v12, v13 offset1:1
	v_add_u32_e32 v2, 0x1080, v0
	v_pk_mul_f32 v[24:25], v[70:71], v[24:25] op_sel_hi:[0,1]
	ds_write2_b32 v2, v22, v23 offset1:1
	v_add_u32_e32 v2, 0x1088, v0
	v_pk_mul_f32 v[18:19], v[68:69], v[18:19] op_sel_hi:[0,1]
	ds_write2_b32 v2, v24, v25 offset1:1
	v_add_u32_e32 v2, 0x14a0, v0
	v_pk_mul_f32 v[20:21], v[68:69], v[20:21] op_sel_hi:[0,1]
	ds_write2_b32 v2, v18, v19 offset1:1
	v_add_u32_e32 v2, 0x14a8, v0
	v_pk_mul_f32 v[30:31], v[66:67], v[30:31] op_sel_hi:[0,1]
	ds_write2_b32 v2, v20, v21 offset1:1
	v_add_u32_e32 v2, 0x18c0, v0
	v_pk_mul_f32 v[32:33], v[66:67], v[32:33] op_sel_hi:[0,1]
	ds_write2_b32 v2, v30, v31 offset1:1
	v_add_u32_e32 v2, 0x18c8, v0
	v_pk_mul_f32 v[28:29], v[64:65], v[28:29] op_sel_hi:[0,1]
	v_pk_mul_f32 v[26:27], v[64:65], v[26:27] op_sel_hi:[0,1]
	ds_write2_b32 v2, v32, v33 offset1:1
	v_add_u32_e32 v2, 0x1ce0, v0
	v_add_u32_e32 v0, 0x1ce8, v0
	ds_write2_b32 v2, v26, v27 offset1:1
	ds_write2_b32 v0, v28, v29 offset1:1
	s_waitcnt lgkmcnt(0)
	s_ashr_i32 s25, s24, 31
	v_lshl_add_u64 v[2:3], s[24:25], 1, v[38:39]
	v_cmp_gt_i32_e32 vcc, s30, v35
	s_and_saveexec_b64 s[4:5], vcc
	s_cbranch_execz .LBB0_51
	ds_read2_b32 v[4:5], v75 offset0:198 offset1:231
	ds_read2_b32 v[8:9], v75 offset0:132 offset1:165
	s_waitcnt lgkmcnt(1)
	v_cvt_pk_bf16_f32 v7, v4, v5
	ds_read2_b32 v[4:5], v75 offset0:66 offset1:99
	s_waitcnt lgkmcnt(1)
	v_cvt_pk_bf16_f32 v6, v8, v9
	ds_read2_b32 v[8:9], v75 offset1:33
	s_waitcnt lgkmcnt(1)
	v_cvt_pk_bf16_f32 v5, v4, v5
	s_waitcnt lgkmcnt(0)
	v_cvt_pk_bf16_f32 v4, v8, v9
	v_add_u32_e32 v8, s22, v35
	v_ashrrev_i32_e32 v9, 31, v8
	v_lshlrev_b64 v[8:9], 12, v[8:9]
	v_lshl_add_u64 v[8:9], v[2:3], 0, v[8:9]
	global_store_dwordx4 v[8:9], v[4:7], off
	s_or_b64 exec, exec, s[4:5]
	v_cmp_gt_i32_e32 vcc, s30, v69
	s_and_saveexec_b64 s[4:5], vcc
	s_cbranch_execnz .LBB0_52

; #define LAS __attribute__((address_space(3)))
; __device__ __forceinline__ unsigned pk2(float lo, float hi) { return f2bf(lo) | (f2bf(hi) << 16); }
; template <int MAPK>
; __device__ __forceinline__ void transpose_item(const float* W, int ldw, int k0, int n0, int ncnt, bf16* WT, int ldd, int dcol0, int moff, LAS float* scr, int lane, const float* gk) {
;     ...
;     const int c = lane & 7;
; #pragma unroll
;     for (int j = 0; j < 4; ++j) { const int n = (lane >> 3) + 8 * j; const LAS float* s = scr + (8 * c) * 33 + n;
;         v4u o; o.x = pk2(s[0 * 33], s[1 * 33]); o.y = pk2(s[2 * 33], s[3 * 33]); o.z = pk2(s[4 * 33], s[5 * 33]); o.w = pk2(s[6 * 33], s[7 * 33]);
;         const int sn = n0 + n - moff;
;         int drow;
;         if (MAPK == MAP_LIN) drow = sn; else if (MAPK == MAP_GATE) drow = 32 * (sn >> 4) + (sn & 15); else drow = 32 * (sn >> 4) + 16 + (sn & 15);
;         if (n < ncnt) *(v4u*)(WT + (size_t)drow * ldd + dcol0 + k0 + 8 * c) = o; }
.LBB0_50:
	ds_read2_b32 v[4:5], v75 offset0:214 offset1:247
	ds_read2_b32 v[8:9], v75 offset0:148 offset1:181
	s_waitcnt lgkmcnt(1)
	v_cvt_pk_bf16_f32 v7, v4, v5
	ds_read2_b32 v[4:5], v75 offset0:82 offset1:115
	s_waitcnt lgkmcnt(1)
	v_cvt_pk_bf16_f32 v6, v8, v9
	ds_read2_b32 v[8:9], v75 offset0:16 offset1:49
	s_waitcnt lgkmcnt(1)
	v_cvt_pk_bf16_f32 v5, v4, v5
	s_waitcnt lgkmcnt(0)
	v_cvt_pk_bf16_f32 v4, v8, v9
	v_add3_u32 v8, s22, v35, 16
	v_ashrrev_i32_e32 v9, 31, v8
	v_lshlrev_b64 v[8:9], 12, v[8:9]
	v_lshl_add_u64 v[8:9], v[2:3], 0, v[8:9]
	global_store_dwordx4 v[8:9], v[4:7], off
	s_or_b64 exec, exec, s[4:5]
	v_cmp_gt_i32_e32 vcc, s30, v73
	s_and_saveexec_b64 s[4:5], vcc
	s_cbranch_execnz .LBB0_54
	s_branch .LBB0_55

; #define LAS __attribute__((address_space(3)))
; __device__ __forceinline__ unsigned pk2(float lo, float hi) { return f2bf(lo) | (f2bf(hi) << 16); }
; template <int MAPK>
; __device__ __forceinline__ void transpose_item(const float* W, int ldw, int k0, int n0, int ncnt, bf16* WT, int ldd, int dcol0, int moff, LAS float* scr, int lane, const float* gk) {
;     ...
;     const int c = lane & 7;
; #pragma unroll
;     for (int j = 0; j < 4; ++j) { const int n = (lane >> 3) + 8 * j; const LAS float* s = scr + (8 * c) * 33 + n;
;         v4u o; o.x = pk2(s[0 * 33], s[1 * 33]); o.y = pk2(s[2 * 33], s[3 * 33]); o.z = pk2(s[4 * 33], s[5 * 33]); o.w = pk2(s[6 * 33], s[7 * 33]);
;         const int sn = n0 + n - moff;
;         int drow;
;         if (MAPK == MAP_LIN) drow = sn; else if (MAPK == MAP_GATE) drow = 32 * (sn >> 4) + (sn & 15); else drow = 32 * (sn >> 4) + 16 + (sn & 15);
;         if (n < ncnt) *(v4u*)(WT + (size_t)drow * ldd + dcol0 + k0 + 8 * c) = o; }
.LBB0_52:
	ds_read2_b32 v[4:5], v75 offset0:206 offset1:239
	ds_read2_b32 v[8:9], v75 offset0:140 offset1:173
	s_waitcnt lgkmcnt(1)
	v_cvt_pk_bf16_f32 v7, v4, v5
	ds_read2_b32 v[4:5], v75 offset0:74 offset1:107
	s_waitcnt lgkmcnt(1)
	v_cvt_pk_bf16_f32 v6, v8, v9
	ds_read2_b32 v[8:9], v75 offset0:8 offset1:41
	s_waitcnt lgkmcnt(1)
	v_cvt_pk_bf16_f32 v5, v4, v5
	s_waitcnt lgkmcnt(0)
	v_cvt_pk_bf16_f32 v4, v8, v9
	v_add3_u32 v8, s22, v35, 8
	v_ashrrev_i32_e32 v9, 31, v8
	v_lshlrev_b64 v[8:9], 12, v[8:9]
	v_lshl_add_u64 v[8:9], v[2:3], 0, v[8:9]
	global_store_dwordx4 v[8:9], v[4:7], off
	s_or_b64 exec, exec, s[4:5]
	v_cmp_gt_i32_e32 vcc, s30, v71
	s_and_saveexec_b64 s[4:5], vcc
	s_cbranch_execnz .LBB0_50

; #define LAS __attribute__((address_space(3)))
; __device__ __forceinline__ unsigned pk2(float lo, float hi) { return f2bf(lo) | (f2bf(hi) << 16); }
; template <int MAPK>
; __device__ __forceinline__ void transpose_item(const float* W, int ldw, int k0, int n0, int ncnt, bf16* WT, int ldd, int dcol0, int moff, LAS float* scr, int lane, const float* gk) {
;     ...
;     const int c = lane & 7;
; #pragma unroll
;     for (int j = 0; j < 4; ++j) { const int n = (lane >> 3) + 8 * j; const LAS float* s = scr + (8 * c) * 33 + n;
;         v4u o; o.x = pk2(s[0 * 33], s[1 * 33]); o.y = pk2(s[2 * 33], s[3 * 33]); o.z = pk2(s[4 * 33], s[5 * 33]); o.w = pk2(s[6 * 33], s[7 * 33]);
;         const int sn = n0 + n - moff;
;         int drow;
;         if (MAPK == MAP_LIN) drow = sn; else if (MAPK == MAP_GATE) drow = 32 * (sn >> 4) + (sn & 15); else drow = 32 * (sn >> 4) + 16 + (sn & 15);
;         if (n < ncnt) *(v4u*)(WT + (size_t)drow * ldd + dcol0 + k0 + 8 * c) = o; }
.LBB0_54:
	ds_read2_b32 v[4:5], v75 offset0:222 offset1:255
	ds_read2_b32 v[8:9], v75 offset0:156 offset1:189
	s_waitcnt lgkmcnt(1)
	v_cvt_pk_bf16_f32 v7, v4, v5
	ds_read2_b32 v[4:5], v75 offset0:90 offset1:123
	s_waitcnt lgkmcnt(1)
	v_cvt_pk_bf16_f32 v6, v8, v9
	ds_read2_b32 v[8:9], v75 offset0:24 offset1:57
	s_waitcnt lgkmcnt(1)
	v_cvt_pk_bf16_f32 v5, v4, v5
	s_waitcnt lgkmcnt(0)
	v_cvt_pk_bf16_f32 v4, v8, v9
	v_add3_u32 v8, s22, v35, 24
	v_ashrrev_i32_e32 v9, 31, v8
	v_lshlrev_b64 v[8:9], 12, v[8:9]
	v_lshl_add_u64 v[2:3], v[2:3], 0, v[8:9]
	global_store_dwordx4 v[2:3], v[4:7], off

; #define LAS __attribute__((address_space(3)))
; #define LDS_WAIT() asm volatile("s_waitcnt lgkmcnt(0)" ::: "memory")
; __device__ __forceinline__ unsigned pk2(float lo, float hi) { return f2bf(lo) | (f2bf(hi) << 16); }
; template <int MAPK>
; __device__ __forceinline__ void transpose_item(const float* W, int ldw, int k0, int n0, int ncnt, bf16* WT, int ldd, int dcol0, int moff, LAS float* scr, int lane, const float* gk) {
;     ...
;       for (int j = 0; j < 8; ++j) v[j] = (c4 < ncnt) ? *(const f32x4*)(wp + (size_t)(8 * j) * ldw) : (f32x4){0.f, 0.f, 0.f, 0.f};
;       asm volatile("" : "+v"(v[0]), "+v"(v[1]), "+v"(v[2]), "+v"(v[3]), "+v"(v[4]), "+v"(v[5]), "+v"(v[6]), "+v"(v[7]) :: "memory");
; #pragma unroll
;       for (int j = 0; j < 8; ++j) v[j] = v[j] * gj[j];
; #pragma unroll
;       for (int j = 0; j < 8; ++j) { LAS float* d = scr + (8 * j + kr) * 33 + c4; d[0] = v[j].x; d[1] = v[j].y; d[2] = v[j].z; d[3] = v[j].w; } }
;     LDS_WAIT(); asm volatile("" ::: "memory");
;     const int c = lane & 7;
; #pragma unroll
;     for (int j = 0; j < 4; ++j) { const int n = (lane >> 3) + 8 * j; const LAS float* s = scr + (8 * c) * 33 + n;
;         v4u o; o.x = pk2(s[0 * 33], s[1 * 33]); o.y = pk2(s[2 * 33], s[3 * 33]); o.z = pk2(s[4 * 33], s[5 * 33]); o.w = pk2(s[6 * 33], s[7 * 33]);
;         const int sn = n0 + n - moff;
;         int drow;
;         if (MAPK == MAP_LIN) drow = sn; else if (MAPK == MAP_GATE) drow = 32 * (sn >> 4) + (sn & 15); else drow = 32 * (sn >> 4) + 16 + (sn & 15);
;         if (n < ncnt) *(v4u*)(WT + (size_t)drow * ldd + dcol0 + k0 + 8 * c) = o; }
.LBB0_78:
	s_or_b64 exec, exec, s[26:27]
	s_waitcnt vmcnt(0)
	v_lshlrev_b32_e32 v91, 2, v35
	ds_bpermute_b32 v78, v91, v90
	ds_bpermute_b32 v76, v91, v90 offset:32
	ds_bpermute_b32 v74, v91, v90 offset:64
	ds_bpermute_b32 v72, v91, v90 offset:96
	ds_bpermute_b32 v70, v91, v90 offset:128
	ds_bpermute_b32 v68, v91, v90 offset:160
	ds_bpermute_b32 v66, v91, v90 offset:192
	ds_bpermute_b32 v64, v91, v90 offset:224
	s_waitcnt lgkmcnt(0)
	v_add_u32_e32 v0, v37, v67
	v_pk_mul_f32 v[2:3], v[78:79], v[2:3] op_sel_hi:[0,1]
	v_pk_mul_f32 v[4:5], v[78:79], v[4:5] op_sel_hi:[0,1]
	v_pk_mul_f32 v[6:7], v[76:77], v[6:7] op_sel_hi:[0,1]
	ds_write2_b32 v0, v2, v3 offset1:1
	ds_write2_b32 v0, v4, v5 offset0:2 offset1:3
	v_add_u32_e32 v2, 0x420, v0
	v_pk_mul_f32 v[8:9], v[76:77], v[8:9] op_sel_hi:[0,1]
	ds_write2_b32 v2, v6, v7 offset1:1
	v_add_u32_e32 v2, 0x428, v0
	v_pk_mul_f32 v[14:15], v[74:75], v[14:15] op_sel_hi:[0,1]
	ds_write2_b32 v2, v8, v9 offset1:1
	v_add_u32_e32 v2, 0x840, v0
	v_pk_mul_f32 v[16:17], v[74:75], v[16:17] op_sel_hi:[0,1]
	ds_write2_b32 v2, v14, v15 offset1:1
	v_add_u32_e32 v2, 0x848, v0
	v_pk_mul_f32 v[10:11], v[72:73], v[10:11] op_sel_hi:[0,1]
	ds_write2_b32 v2, v16, v17 offset1:1
	v_add_u32_e32 v2, 0xc60, v0
	v_pk_mul_f32 v[12:13], v[72:73], v[12:13] op_sel_hi:[0,1]
	ds_write2_b32 v2, v10, v11 offset1:1
	v_add_u32_e32 v2, 0xc68, v0
	v_pk_mul_f32 v[22:23], v[70:71], v[22:23] op_sel_hi:[0,1]
	ds_write2_b32 v2, v12, v13 offset1:1
	v_add_u32_e32 v2, 0x1080, v0
	v_pk_mul_f32 v[24:25], v[70:71], v[24:25] op_sel_hi:[0,1]
	ds_write2_b32 v2, v22, v23 offset1:1
	v_add_u32_e32 v2, 0x1088, v0
	v_pk_mul_f32 v[18:19], v[68:69], v[18:19] op_sel_hi:[0,1]
	ds_write2_b32 v2, v24, v25 offset1:1
	v_add_u32_e32 v2, 0x14a0, v0
	v_pk_mul_f32 v[20:21], v[68:69], v[20:21] op_sel_hi:[0,1]
	ds_write2_b32 v2, v18, v19 offset1:1
	v_add_u32_e32 v2, 0x14a8, v0
	v_pk_mul_f32 v[30:31], v[66:67], v[30:31] op_sel_hi:[0,1]
	ds_write2_b32 v2, v20, v21 offset1:1
	v_add_u32_e32 v2, 0x18c0, v0
	v_pk_mul_f32 v[32:33], v[66:67], v[32:33] op_sel_hi:[0,1]
	ds_write2_b32 v2, v30, v31 offset1:1
	v_add_u32_e32 v2, 0x18c8, v0
	v_pk_mul_f32 v[28:29], v[64:65], v[28:29] op_sel_hi:[0,1]
	v_pk_mul_f32 v[26:27], v[64:65], v[26:27] op_sel_hi:[0,1]
	ds_write2_b32 v2, v32, v33 offset1:1
	v_add_u32_e32 v2, 0x1ce0, v0
	v_add_u32_e32 v0, 0x1ce8, v0
	ds_write2_b32 v2, v26, v27 offset1:1
	ds_write2_b32 v0, v28, v29 offset1:1
	s_waitcnt lgkmcnt(0)
	s_ashr_i32 s23, s22, 31
	s_addk_i32 s24, 0x1400
	v_lshl_add_u64 v[2:3], s[22:23], 1, v[38:39]
	v_cmp_gt_i32_e32 vcc, s31, v35
	s_and_saveexec_b64 s[4:5], vcc
	s_cbranch_execz .LBB0_82
	ds_read2_b32 v[4:5], v75 offset0:198 offset1:231
	ds_read2_b32 v[8:9], v75 offset0:132 offset1:165
	s_waitcnt lgkmcnt(1)
	v_cvt_pk_bf16_f32 v7, v4, v5
	ds_read2_b32 v[4:5], v75 offset0:66 offset1:99
	s_waitcnt lgkmcnt(1)
	v_cvt_pk_bf16_f32 v6, v8, v9
	ds_read2_b32 v[8:9], v75 offset1:33
	s_waitcnt lgkmcnt(1)
	v_cvt_pk_bf16_f32 v5, v4, v5
	s_waitcnt lgkmcnt(0)
	v_cvt_pk_bf16_f32 v4, v8, v9
	v_or_b32_e32 v8, s24, v35
	v_ashrrev_i32_e32 v9, 31, v8
	v_lshlrev_b64 v[8:9], 12, v[8:9]
	v_lshl_add_u64 v[8:9], v[2:3], 0, v[8:9]
	global_store_dwordx4 v[8:9], v[4:7], off
	s_or_b64 exec, exec, s[4:5]
	v_cmp_gt_i32_e32 vcc, s31, v69
	s_and_saveexec_b64 s[4:5], vcc
	s_cbranch_execnz .LBB0_83

; #define LAS __attribute__((address_space(3)))
; __device__ __forceinline__ unsigned pk2(float lo, float hi) { return f2bf(lo) | (f2bf(hi) << 16); }
; template <int MAPK>
; __device__ __forceinline__ void transpose_item(const float* W, int ldw, int k0, int n0, int ncnt, bf16* WT, int ldd, int dcol0, int moff, LAS float* scr, int lane, const float* gk) {
;     ...
;     const int c = lane & 7;
; #pragma unroll
;     for (int j = 0; j < 4; ++j) { const int n = (lane >> 3) + 8 * j; const LAS float* s = scr + (8 * c) * 33 + n;
;         v4u o; o.x = pk2(s[0 * 33], s[1 * 33]); o.y = pk2(s[2 * 33], s[3 * 33]); o.z = pk2(s[4 * 33], s[5 * 33]); o.w = pk2(s[6 * 33], s[7 * 33]);
;         const int sn = n0 + n - moff;
;         int drow;
;         if (MAPK == MAP_LIN) drow = sn; else if (MAPK == MAP_GATE) drow = 32 * (sn >> 4) + (sn & 15); else drow = 32 * (sn >> 4) + 16 + (sn & 15);
;         if (n < ncnt) *(v4u*)(WT + (size_t)drow * ldd + dcol0 + k0 + 8 * c) = o; }
.LBB0_81:
	ds_read2_b32 v[4:5], v75 offset0:214 offset1:247
	ds_read2_b32 v[8:9], v75 offset0:148 offset1:181
	s_waitcnt lgkmcnt(1)
	v_cvt_pk_bf16_f32 v7, v4, v5
	ds_read2_b32 v[4:5], v75 offset0:82 offset1:115
	s_waitcnt lgkmcnt(1)
	v_cvt_pk_bf16_f32 v6, v8, v9
	ds_read2_b32 v[8:9], v75 offset0:16 offset1:49
	s_waitcnt lgkmcnt(1)
	v_cvt_pk_bf16_f32 v5, v4, v5
	s_waitcnt lgkmcnt(0)
	v_cvt_pk_bf16_f32 v4, v8, v9
	v_or_b32_e32 v8, s24, v71
	v_ashrrev_i32_e32 v9, 31, v8
	v_lshlrev_b64 v[8:9], 12, v[8:9]
	v_lshl_add_u64 v[8:9], v[2:3], 0, v[8:9]
	global_store_dwordx4 v[8:9], v[4:7], off
	s_or_b64 exec, exec, s[4:5]
	v_cmp_gt_i32_e32 vcc, s31, v73
	s_and_saveexec_b64 s[4:5], vcc
	s_cbranch_execnz .LBB0_85
	s_branch .LBB0_86

; #define LAS __attribute__((address_space(3)))
; __device__ __forceinline__ unsigned pk2(float lo, float hi) { return f2bf(lo) | (f2bf(hi) << 16); }
; template <int MAPK>
; __device__ __forceinline__ void transpose_item(const float* W, int ldw, int k0, int n0, int ncnt, bf16* WT, int ldd, int dcol0, int moff, LAS float* scr, int lane, const float* gk) {
;     ...
;     const int c = lane & 7;
; #pragma unroll
;     for (int j = 0; j < 4; ++j) { const int n = (lane >> 3) + 8 * j; const LAS float* s = scr + (8 * c) * 33 + n;
;         v4u o; o.x = pk2(s[0 * 33], s[1 * 33]); o.y = pk2(s[2 * 33], s[3 * 33]); o.z = pk2(s[4 * 33], s[5 * 33]); o.w = pk2(s[6 * 33], s[7 * 33]);
;         const int sn = n0 + n - moff;
;         int drow;
;         if (MAPK == MAP_LIN) drow = sn; else if (MAPK == MAP_GATE) drow = 32 * (sn >> 4) + (sn & 15); else drow = 32 * (sn >> 4) + 16 + (sn & 15);
;         if (n < ncnt) *(v4u*)(WT + (size_t)drow * ldd + dcol0 + k0 + 8 * c) = o; }
.LBB0_83:
	ds_read2_b32 v[4:5], v75 offset0:206 offset1:239
	ds_read2_b32 v[8:9], v75 offset0:140 offset1:173
	s_waitcnt lgkmcnt(1)
	v_cvt_pk_bf16_f32 v7, v4, v5
	ds_read2_b32 v[4:5], v75 offset0:74 offset1:107
	s_waitcnt lgkmcnt(1)
	v_cvt_pk_bf16_f32 v6, v8, v9
	ds_read2_b32 v[8:9], v75 offset0:8 offset1:41
	s_waitcnt lgkmcnt(1)
	v_cvt_pk_bf16_f32 v5, v4, v5
	s_waitcnt lgkmcnt(0)
	v_cvt_pk_bf16_f32 v4, v8, v9
	v_or_b32_e32 v8, s24, v69
	v_ashrrev_i32_e32 v9, 31, v8
	v_lshlrev_b64 v[8:9], 12, v[8:9]
	v_lshl_add_u64 v[8:9], v[2:3], 0, v[8:9]
	global_store_dwordx4 v[8:9], v[4:7], off
	s_or_b64 exec, exec, s[4:5]
	v_cmp_gt_i32_e32 vcc, s31, v71
	s_and_saveexec_b64 s[4:5], vcc
	s_cbranch_execnz .LBB0_81

; #define LAS __attribute__((address_space(3)))
; __device__ __forceinline__ unsigned pk2(float lo, float hi) { return f2bf(lo) | (f2bf(hi) << 16); }
; template <int MAPK>
; __device__ __forceinline__ void transpose_item(const float* W, int ldw, int k0, int n0, int ncnt, bf16* WT, int ldd, int dcol0, int moff, LAS float* scr, int lane, const float* gk) {
;     ...
;     const int c = lane & 7;
; #pragma unroll
;     for (int j = 0; j < 4; ++j) { const int n = (lane >> 3) + 8 * j; const LAS float* s = scr + (8 * c) * 33 + n;
;         v4u o; o.x = pk2(s[0 * 33], s[1 * 33]); o.y = pk2(s[2 * 33], s[3 * 33]); o.z = pk2(s[4 * 33], s[5 * 33]); o.w = pk2(s[6 * 33], s[7 * 33]);
;         const int sn = n0 + n - moff;
;         int drow;
;         if (MAPK == MAP_LIN) drow = sn; else if (MAPK == MAP_GATE) drow = 32 * (sn >> 4) + (sn & 15); else drow = 32 * (sn >> 4) + 16 + (sn & 15);
;         if (n < ncnt) *(v4u*)(WT + (size_t)drow * ldd + dcol0 + k0 + 8 * c) = o; }
.LBB0_85:
	ds_read2_b32 v[4:5], v75 offset0:222 offset1:255
	ds_read2_b32 v[8:9], v75 offset0:156 offset1:189
	s_waitcnt lgkmcnt(1)
	v_cvt_pk_bf16_f32 v7, v4, v5
	ds_read2_b32 v[4:5], v75 offset0:90 offset1:123
	s_waitcnt lgkmcnt(1)
	v_cvt_pk_bf16_f32 v6, v8, v9
	ds_read2_b32 v[8:9], v75 offset0:24 offset1:57
	s_waitcnt lgkmcnt(1)
	v_cvt_pk_bf16_f32 v5, v4, v5
	s_waitcnt lgkmcnt(0)
	v_cvt_pk_bf16_f32 v4, v8, v9
	v_or_b32_e32 v8, s24, v73
	v_ashrrev_i32_e32 v9, 31, v8
	v_lshlrev_b64 v[8:9], 12, v[8:9]
	v_lshl_add_u64 v[2:3], v[2:3], 0, v[8:9]
	global_store_dwordx4 v[2:3], v[4:7], off

; #define LAS __attribute__((address_space(3)))
; #define LDS_WAIT() asm volatile("s_waitcnt lgkmcnt(0)" ::: "memory")
; __device__ __forceinline__ unsigned pk2(float lo, float hi) { return f2bf(lo) | (f2bf(hi) << 16); }
; template <int MAPK>
; __device__ __forceinline__ void transpose_item(const float* W, int ldw, int k0, int n0, int ncnt, bf16* WT, int ldd, int dcol0, int moff, LAS float* scr, int lane, const float* gk) {
;     ...
;           for (int j = 0; j < 8; ++j) gj[j] = gk[k0 + 8 * j + kr]; }
; #pragma unroll
;       for (int j = 0; j < 8; ++j) v[j] = (c4 < ncnt) ? *(const f32x4*)(wp + (size_t)(8 * j) * ldw) : (f32x4){0.f, 0.f, 0.f, 0.f};
;       asm volatile("" : "+v"(v[0]), "+v"(v[1]), "+v"(v[2]), "+v"(v[3]), "+v"(v[4]), "+v"(v[5]), "+v"(v[6]), "+v"(v[7]) :: "memory");
; #pragma unroll
;       for (int j = 0; j < 8; ++j) v[j] = v[j] * gj[j];
; #pragma unroll
;       for (int j = 0; j < 8; ++j) { LAS float* d = scr + (8 * j + kr) * 33 + c4; d[0] = v[j].x; d[1] = v[j].y; d[2] = v[j].z; d[3] = v[j].w; } }
;     LDS_WAIT(); asm volatile("" ::: "memory");
;     const int c = lane & 7;
; #pragma unroll
;     for (int j = 0; j < 4; ++j) { const int n = (lane >> 3) + 8 * j; const LAS float* s = scr + (8 * c) * 33 + n;
;         v4u o; o.x = pk2(s[0 * 33], s[1 * 33]); o.y = pk2(s[2 * 33], s[3 * 33]); o.z = pk2(s[4 * 33], s[5 * 33]); o.w = pk2(s[6 * 33], s[7 * 33]);
;         const int sn = n0 + n - moff;
;         int drow;
;         if (MAPK == MAP_LIN) drow = sn; else if (MAPK == MAP_GATE) drow = 32 * (sn >> 4) + (sn & 15); else drow = 32 * (sn >> 4) + 16 + (sn & 15);
;         if (n < ncnt) *(v4u*)(WT + (size_t)drow * ldd + dcol0 + k0 + 8 * c) = o; }
.LBB0_109:
	s_or_b64 exec, exec, s[26:27]
	s_waitcnt vmcnt(0)
	v_lshlrev_b32_e32 v91, 2, v35
	ds_bpermute_b32 v78, v91, v90
	ds_bpermute_b32 v76, v91, v90 offset:32
	ds_bpermute_b32 v74, v91, v90 offset:64
	ds_bpermute_b32 v72, v91, v90 offset:96
	ds_bpermute_b32 v70, v91, v90 offset:128
	ds_bpermute_b32 v68, v91, v90 offset:160
	ds_bpermute_b32 v66, v91, v90 offset:192
	ds_bpermute_b32 v64, v91, v90 offset:224
	s_waitcnt lgkmcnt(0)
	v_add_u32_e32 v0, v37, v67
	v_pk_mul_f32 v[2:3], v[78:79], v[2:3] op_sel_hi:[0,1]
	v_pk_mul_f32 v[4:5], v[78:79], v[4:5] op_sel_hi:[0,1]
	v_pk_mul_f32 v[6:7], v[76:77], v[6:7] op_sel_hi:[0,1]
	ds_write2_b32 v0, v2, v3 offset1:1
	ds_write2_b32 v0, v4, v5 offset0:2 offset1:3
	v_add_u32_e32 v2, 0x420, v0
	v_pk_mul_f32 v[8:9], v[76:77], v[8:9] op_sel_hi:[0,1]
	ds_write2_b32 v2, v6, v7 offset1:1
	v_add_u32_e32 v2, 0x428, v0
	v_pk_mul_f32 v[14:15], v[74:75], v[14:15] op_sel_hi:[0,1]
	ds_write2_b32 v2, v8, v9 offset1:1
	v_add_u32_e32 v2, 0x840, v0
	v_pk_mul_f32 v[16:17], v[74:75], v[16:17] op_sel_hi:[0,1]
	ds_write2_b32 v2, v14, v15 offset1:1
	v_add_u32_e32 v2, 0x848, v0
	v_pk_mul_f32 v[10:11], v[72:73], v[10:11] op_sel_hi:[0,1]
	ds_write2_b32 v2, v16, v17 offset1:1
	v_add_u32_e32 v2, 0xc60, v0
	v_pk_mul_f32 v[12:13], v[72:73], v[12:13] op_sel_hi:[0,1]
	ds_write2_b32 v2, v10, v11 offset1:1
	v_add_u32_e32 v2, 0xc68, v0
	v_pk_mul_f32 v[22:23], v[70:71], v[22:23] op_sel_hi:[0,1]
	ds_write2_b32 v2, v12, v13 offset1:1
	v_add_u32_e32 v2, 0x1080, v0
	v_pk_mul_f32 v[24:25], v[70:71], v[24:25] op_sel_hi:[0,1]
	ds_write2_b32 v2, v22, v23 offset1:1
	v_add_u32_e32 v2, 0x1088, v0
	v_pk_mul_f32 v[18:19], v[68:69], v[18:19] op_sel_hi:[0,1]
	ds_write2_b32 v2, v24, v25 offset1:1
	v_add_u32_e32 v2, 0x14a0, v0
	v_pk_mul_f32 v[20:21], v[68:69], v[20:21] op_sel_hi:[0,1]
	ds_write2_b32 v2, v18, v19 offset1:1
	v_add_u32_e32 v2, 0x14a8, v0
	v_pk_mul_f32 v[30:31], v[66:67], v[30:31] op_sel_hi:[0,1]
	ds_write2_b32 v2, v20, v21 offset1:1
	v_add_u32_e32 v2, 0x18c0, v0
	v_pk_mul_f32 v[32:33], v[66:67], v[32:33] op_sel_hi:[0,1]
	ds_write2_b32 v2, v30, v31 offset1:1
	v_add_u32_e32 v2, 0x18c8, v0
	v_pk_mul_f32 v[28:29], v[64:65], v[28:29] op_sel_hi:[0,1]
	v_pk_mul_f32 v[26:27], v[64:65], v[26:27] op_sel_hi:[0,1]
	ds_write2_b32 v2, v32, v33 offset1:1
	v_add_u32_e32 v2, 0x1ce0, v0
	v_add_u32_e32 v0, 0x1ce8, v0
	ds_write2_b32 v2, v26, v27 offset1:1
	ds_write2_b32 v0, v28, v29 offset1:1
	s_waitcnt lgkmcnt(0)
	s_ashr_i32 s23, s22, 31
	s_addk_i32 s24, 0x1800
	v_lshl_add_u64 v[2:3], s[22:23], 1, v[38:39]
	v_cmp_gt_i32_e32 vcc, s30, v35
	s_and_saveexec_b64 s[4:5], vcc
	s_cbranch_execz .LBB0_113
	ds_read2_b32 v[4:5], v75 offset0:198 offset1:231
	ds_read2_b32 v[8:9], v75 offset0:132 offset1:165
	s_waitcnt lgkmcnt(1)
	v_cvt_pk_bf16_f32 v7, v4, v5
	ds_read2_b32 v[4:5], v75 offset0:66 offset1:99
	s_waitcnt lgkmcnt(1)
	v_cvt_pk_bf16_f32 v6, v8, v9
	ds_read2_b32 v[8:9], v75 offset1:33
	s_waitcnt lgkmcnt(1)
	v_cvt_pk_bf16_f32 v5, v4, v5
	s_waitcnt lgkmcnt(0)
	v_cvt_pk_bf16_f32 v4, v8, v9
	v_or_b32_e32 v8, s24, v35
	v_ashrrev_i32_e32 v9, 31, v8
	v_lshlrev_b64 v[8:9], 12, v[8:9]
	v_lshl_add_u64 v[8:9], v[2:3], 0, v[8:9]
	global_store_dwordx4 v[8:9], v[4:7], off
	s_or_b64 exec, exec, s[4:5]
	v_cmp_gt_i32_e32 vcc, s30, v69
	s_and_saveexec_b64 s[4:5], vcc
	s_cbranch_execnz .LBB0_114

; #define LAS __attribute__((address_space(3)))
; __device__ __forceinline__ unsigned pk2(float lo, float hi) { return f2bf(lo) | (f2bf(hi) << 16); }
; template <int MAPK>
; __device__ __forceinline__ void transpose_item(const float* W, int ldw, int k0, int n0, int ncnt, bf16* WT, int ldd, int dcol0, int moff, LAS float* scr, int lane, const float* gk) {
;     ...
;     const int c = lane & 7;
; #pragma unroll
;     for (int j = 0; j < 4; ++j) { const int n = (lane >> 3) + 8 * j; const LAS float* s = scr + (8 * c) * 33 + n;
;         v4u o; o.x = pk2(s[0 * 33], s[1 * 33]); o.y = pk2(s[2 * 33], s[3 * 33]); o.z = pk2(s[4 * 33], s[5 * 33]); o.w = pk2(s[6 * 33], s[7 * 33]);
;         const int sn = n0 + n - moff;
;         int drow;
;         if (MAPK == MAP_LIN) drow = sn; else if (MAPK == MAP_GATE) drow = 32 * (sn >> 4) + (sn & 15); else drow = 32 * (sn >> 4) + 16 + (sn & 15);
;         if (n < ncnt) *(v4u*)(WT + (size_t)drow * ldd + dcol0 + k0 + 8 * c) = o; }
.LBB0_112:
	ds_read2_b32 v[4:5], v75 offset0:214 offset1:247
	ds_read2_b32 v[8:9], v75 offset0:148 offset1:181
	s_waitcnt lgkmcnt(1)
	v_cvt_pk_bf16_f32 v7, v4, v5
	ds_read2_b32 v[4:5], v75 offset0:82 offset1:115
	s_waitcnt lgkmcnt(1)
	v_cvt_pk_bf16_f32 v6, v8, v9
	ds_read2_b32 v[8:9], v75 offset0:16 offset1:49
	s_waitcnt lgkmcnt(1)
	v_cvt_pk_bf16_f32 v5, v4, v5
	s_waitcnt lgkmcnt(0)
	v_cvt_pk_bf16_f32 v4, v8, v9
	v_or_b32_e32 v8, s24, v71
	v_ashrrev_i32_e32 v9, 31, v8
	v_lshlrev_b64 v[8:9], 12, v[8:9]
	v_lshl_add_u64 v[8:9], v[2:3], 0, v[8:9]
	global_store_dwordx4 v[8:9], v[4:7], off
	s_or_b64 exec, exec, s[4:5]
	v_cmp_gt_i32_e32 vcc, s30, v73
	s_and_saveexec_b64 s[4:5], vcc
	s_cbranch_execnz .LBB0_116
	s_branch .LBB0_117

; #define LAS __attribute__((address_space(3)))
; __device__ __forceinline__ unsigned pk2(float lo, float hi) { return f2bf(lo) | (f2bf(hi) << 16); }
; template <int MAPK>
; __device__ __forceinline__ void transpose_item(const float* W, int ldw, int k0, int n0, int ncnt, bf16* WT, int ldd, int dcol0, int moff, LAS float* scr, int lane, const float* gk) {
;     ...
;     const int c = lane & 7;
; #pragma unroll
;     for (int j = 0; j < 4; ++j) { const int n = (lane >> 3) + 8 * j; const LAS float* s = scr + (8 * c) * 33 + n;
;         v4u o; o.x = pk2(s[0 * 33], s[1 * 33]); o.y = pk2(s[2 * 33], s[3 * 33]); o.z = pk2(s[4 * 33], s[5 * 33]); o.w = pk2(s[6 * 33], s[7 * 33]);
;         const int sn = n0 + n - moff;
;         int drow;
;         if (MAPK == MAP_LIN) drow = sn; else if (MAPK == MAP_GATE) drow = 32 * (sn >> 4) + (sn & 15); else drow = 32 * (sn >> 4) + 16 + (sn & 15);
;         if (n < ncnt) *(v4u*)(WT + (size_t)drow * ldd + dcol0 + k0 + 8 * c) = o; }
.LBB0_114:
	ds_read2_b32 v[4:5], v75 offset0:206 offset1:239
	ds_read2_b32 v[8:9], v75 offset0:140 offset1:173
	s_waitcnt lgkmcnt(1)
	v_cvt_pk_bf16_f32 v7, v4, v5
	ds_read2_b32 v[4:5], v75 offset0:74 offset1:107
	s_waitcnt lgkmcnt(1)
	v_cvt_pk_bf16_f32 v6, v8, v9
	ds_read2_b32 v[8:9], v75 offset0:8 offset1:41
	s_waitcnt lgkmcnt(1)
	v_cvt_pk_bf16_f32 v5, v4, v5
	s_waitcnt lgkmcnt(0)
	v_cvt_pk_bf16_f32 v4, v8, v9
	v_or_b32_e32 v8, s24, v69
	v_ashrrev_i32_e32 v9, 31, v8
	v_lshlrev_b64 v[8:9], 12, v[8:9]
	v_lshl_add_u64 v[8:9], v[2:3], 0, v[8:9]
	global_store_dwordx4 v[8:9], v[4:7], off
	s_or_b64 exec, exec, s[4:5]
	v_cmp_gt_i32_e32 vcc, s30, v71
	s_and_saveexec_b64 s[4:5], vcc
	s_cbranch_execnz .LBB0_112

; #define LAS __attribute__((address_space(3)))
; #define LDS_WAIT() asm volatile("s_waitcnt lgkmcnt(0)" ::: "memory")
; __device__ __forceinline__ unsigned pk2(float lo, float hi) { return f2bf(lo) | (f2bf(hi) << 16); }
; template <int MAPK>
; __device__ __forceinline__ void transpose_item(const float* W, int ldw, int k0, int n0, int ncnt, bf16* WT, int ldd, int dcol0, int moff, LAS float* scr, int lane, const float* gk) {
;     ...
;           for (int j = 0; j < 8; ++j) gj[j] = gk[k0 + 8 * j + kr]; }
; #pragma unroll
;       for (int j = 0; j < 8; ++j) v[j] = (c4 < ncnt) ? *(const f32x4*)(wp + (size_t)(8 * j) * ldw) : (f32x4){0.f, 0.f, 0.f, 0.f};
;       asm volatile("" : "+v"(v[0]), "+v"(v[1]), "+v"(v[2]), "+v"(v[3]), "+v"(v[4]), "+v"(v[5]), "+v"(v[6]), "+v"(v[7]) :: "memory");
; #pragma unroll
;       for (int j = 0; j < 8; ++j) v[j] = v[j] * gj[j];
; #pragma unroll
;       for (int j = 0; j < 8; ++j) { LAS float* d = scr + (8 * j + kr) * 33 + c4; d[0] = v[j].x; d[1] = v[j].y; d[2] = v[j].z; d[3] = v[j].w; } }
;     LDS_WAIT(); asm volatile("" ::: "memory");
;     const int c = lane & 7;
; #pragma unroll
;     for (int j = 0; j < 4; ++j) { const int n = (lane >> 3) + 8 * j; const LAS float* s = scr + (8 * c) * 33 + n;
;         v4u o; o.x = pk2(s[0 * 33], s[1 * 33]); o.y = pk2(s[2 * 33], s[3 * 33]); o.z = pk2(s[4 * 33], s[5 * 33]); o.w = pk2(s[6 * 33], s[7 * 33]);
;         const int sn = n0 + n - moff;
;         int drow;
;         if (MAPK == MAP_LIN) drow = sn; else if (MAPK == MAP_GATE) drow = 32 * (sn >> 4) + (sn & 15); else drow = 32 * (sn >> 4) + 16 + (sn & 15);
;         if (n < ncnt) *(v4u*)(WT + (size_t)drow * ldd + dcol0 + k0 + 8 * c) = o; }
.LBB0_140:
	s_or_b64 exec, exec, s[22:23]
	s_waitcnt vmcnt(0)
	v_lshlrev_b32_e32 v91, 2, v35
	ds_bpermute_b32 v78, v91, v90
	ds_bpermute_b32 v76, v91, v90 offset:32
	ds_bpermute_b32 v74, v91, v90 offset:64
	ds_bpermute_b32 v72, v91, v90 offset:96
	ds_bpermute_b32 v70, v91, v90 offset:128
	ds_bpermute_b32 v68, v91, v90 offset:160
	ds_bpermute_b32 v66, v91, v90 offset:192
	ds_bpermute_b32 v64, v91, v90 offset:224
	s_waitcnt lgkmcnt(0)
	v_add_u32_e32 v0, v37, v67
	v_pk_mul_f32 v[2:3], v[78:79], v[2:3] op_sel_hi:[0,1]
	v_pk_mul_f32 v[4:5], v[78:79], v[4:5] op_sel_hi:[0,1]
	v_pk_mul_f32 v[6:7], v[76:77], v[6:7] op_sel_hi:[0,1]
	ds_write2_b32 v0, v2, v3 offset1:1
	ds_write2_b32 v0, v4, v5 offset0:2 offset1:3
	v_add_u32_e32 v2, 0x420, v0
	v_pk_mul_f32 v[8:9], v[76:77], v[8:9] op_sel_hi:[0,1]
	ds_write2_b32 v2, v6, v7 offset1:1
	v_add_u32_e32 v2, 0x428, v0
	v_pk_mul_f32 v[14:15], v[74:75], v[14:15] op_sel_hi:[0,1]
	ds_write2_b32 v2, v8, v9 offset1:1
	v_add_u32_e32 v2, 0x840, v0
	v_pk_mul_f32 v[16:17], v[74:75], v[16:17] op_sel_hi:[0,1]
	ds_write2_b32 v2, v14, v15 offset1:1
	v_add_u32_e32 v2, 0x848, v0
	v_pk_mul_f32 v[10:11], v[72:73], v[10:11] op_sel_hi:[0,1]
	ds_write2_b32 v2, v16, v17 offset1:1
	v_add_u32_e32 v2, 0xc60, v0
	v_pk_mul_f32 v[12:13], v[72:73], v[12:13] op_sel_hi:[0,1]
	ds_write2_b32 v2, v10, v11 offset1:1
	v_add_u32_e32 v2, 0xc68, v0
	v_pk_mul_f32 v[22:23], v[70:71], v[22:23] op_sel_hi:[0,1]
	ds_write2_b32 v2, v12, v13 offset1:1
	v_add_u32_e32 v2, 0x1080, v0
	v_pk_mul_f32 v[24:25], v[70:71], v[24:25] op_sel_hi:[0,1]
	ds_write2_b32 v2, v22, v23 offset1:1
	v_add_u32_e32 v2, 0x1088, v0
	v_pk_mul_f32 v[18:19], v[68:69], v[18:19] op_sel_hi:[0,1]
	ds_write2_b32 v2, v24, v25 offset1:1
	v_add_u32_e32 v2, 0x14a0, v0
	v_pk_mul_f32 v[20:21], v[68:69], v[20:21] op_sel_hi:[0,1]
	ds_write2_b32 v2, v18, v19 offset1:1
	v_add_u32_e32 v2, 0x14a8, v0
	v_pk_mul_f32 v[30:31], v[66:67], v[30:31] op_sel_hi:[0,1]
	ds_write2_b32 v2, v20, v21 offset1:1
	v_add_u32_e32 v2, 0x18c0, v0
	v_pk_mul_f32 v[32:33], v[66:67], v[32:33] op_sel_hi:[0,1]
	ds_write2_b32 v2, v30, v31 offset1:1
	v_add_u32_e32 v2, 0x18c8, v0
	v_pk_mul_f32 v[28:29], v[64:65], v[28:29] op_sel_hi:[0,1]
	v_pk_mul_f32 v[26:27], v[64:65], v[26:27] op_sel_hi:[0,1]
	ds_write2_b32 v2, v32, v33 offset1:1
	v_add_u32_e32 v2, 0x1ce0, v0
	v_add_u32_e32 v0, 0x1ce8, v0
	ds_write2_b32 v2, v26, v27 offset1:1
	ds_write2_b32 v0, v28, v29 offset1:1
	s_waitcnt lgkmcnt(0)
	ds_read2_b32 v[6:7], v75 offset0:231 offset1:239
	ds_read2_b32 v[8:9], v75 offset0:198 offset1:206
	ds_read2_b32 v[12:13], v75 offset0:132 offset1:140
	ds_read2_b32 v[10:11], v75 offset0:165 offset1:173
	ds_read2_b32 v[16:17], v75 offset0:66 offset1:74
	s_waitcnt lgkmcnt(4)
	s_waitcnt lgkmcnt(3)
	ds_read2_b32 v[14:15], v75 offset0:99 offset1:107
	v_cvt_pk_bf16_f32 v5, v8, v6
	s_waitcnt lgkmcnt(3)
	s_waitcnt lgkmcnt(2)
	ds_read2_b32 v[20:21], v75 offset1:8
	ds_read2_b32 v[18:19], v75 offset0:33 offset1:41
	v_cvt_pk_bf16_f32 v4, v12, v10
	s_waitcnt lgkmcnt(3)
	s_waitcnt lgkmcnt(2)
	s_ashr_i32 s21, s20, 31
	v_cvt_pk_bf16_f32 v3, v16, v14
	s_waitcnt lgkmcnt(1)
	s_waitcnt lgkmcnt(0)
	v_lshl_add_u64 v[22:23], s[20:21], 1, v[62:63]
	s_mov_b32 s20, 0x1c40000
	v_add_co_u32_e32 v24, vcc, s20, v22
	v_cvt_pk_bf16_f32 v2, v20, v18
	s_nop 0
	v_addc_co_u32_e32 v25, vcc, 0, v23, vcc
	global_store_dwordx4 v[24:25], v[2:5], off
	s_nop 1
	v_cvt_pk_bf16_f32 v5, v9, v7
	s_nop 0
	v_cvt_pk_bf16_f32 v4, v13, v11
	v_cvt_pk_bf16_f32 v3, v17, v15
	v_add_co_u32_e32 v6, vcc, 0x1c48000, v22
	v_cvt_pk_bf16_f32 v2, v21, v19
	s_nop 0
	v_addc_co_u32_e32 v7, vcc, 0, v23, vcc
	global_store_dwordx4 v[6:7], v[2:5], off
	s_waitcnt lgkmcnt(0)
	s_mov_b32 s30, s24
	s_andn2_b64 vcc, exec, s[4:5]
	s_cbranch_vccnz .LBB0_24

; #define LAS __attribute__((address_space(3)))
; #define LDS_WAIT() asm volatile("s_waitcnt lgkmcnt(0)" ::: "memory")
; __device__ __forceinline__ unsigned pk2(float lo, float hi) { return f2bf(lo) | (f2bf(hi) << 16); }
; template <int MAPK>
; __device__ __forceinline__ void transpose_item(const float* W, int ldw, int k0, int n0, int ncnt, bf16* WT, int ldd, int dcol0, int moff, LAS float* scr, int lane, const float* gk) {
;     ...
;       for (int j = 0; j < 8; ++j) { LAS float* d = scr + (8 * j + kr) * 33 + c4; d[0] = v[j].x; d[1] = v[j].y; d[2] = v[j].z; d[3] = v[j].w; } }
;     LDS_WAIT(); asm volatile("" ::: "memory");
;     const int c = lane & 7;
; #pragma unroll
;     for (int j = 0; j < 4; ++j) { const int n = (lane >> 3) + 8 * j; const LAS float* s = scr + (8 * c) * 33 + n;
;         v4u o; o.x = pk2(s[0 * 33], s[1 * 33]); o.y = pk2(s[2 * 33], s[3 * 33]); o.z = pk2(s[4 * 33], s[5 * 33]); o.w = pk2(s[6 * 33], s[7 * 33]);
;         const int sn = n0 + n - moff;
;         int drow;
;         if (MAPK == MAP_LIN) drow = sn; else if (MAPK == MAP_GATE) drow = 32 * (sn >> 4) + (sn & 15); else drow = 32 * (sn >> 4) + 16 + (sn & 15);
;         if (n < ncnt) *(v4u*)(WT + (size_t)drow * ldd + dcol0 + k0 + 8 * c) = o; }
.LBB0_190:
	s_or_b64 exec, exec, s[26:27]
	s_waitcnt vmcnt(0)
	v_add_u32_e32 v0, v37, v67
	v_add_u32_e32 v64, 0x420, v0
	s_ashr_i32 s25, s24, 31
	ds_write2_b32 v0, v2, v3 offset1:1
	ds_write2_b32 v0, v4, v5 offset0:2 offset1:3
	ds_write2_b32 v64, v6, v7 offset1:1
	v_add_u32_e32 v2, 0x428, v0
	ds_write2_b32 v2, v8, v9 offset1:1
	v_add_u32_e32 v2, 0x840, v0
	ds_write2_b32 v2, v14, v15 offset1:1
	v_add_u32_e32 v2, 0x848, v0
	ds_write2_b32 v2, v16, v17 offset1:1
	v_add_u32_e32 v2, 0xc60, v0
	ds_write2_b32 v2, v10, v11 offset1:1
	v_add_u32_e32 v2, 0xc68, v0
	ds_write2_b32 v2, v12, v13 offset1:1
	v_add_u32_e32 v2, 0x1080, v0
	ds_write2_b32 v2, v22, v23 offset1:1
	v_add_u32_e32 v2, 0x1088, v0
	ds_write2_b32 v2, v24, v25 offset1:1
	v_add_u32_e32 v2, 0x14a0, v0
	ds_write2_b32 v2, v18, v19 offset1:1
	v_add_u32_e32 v2, 0x14a8, v0
	ds_write2_b32 v2, v20, v21 offset1:1
	v_add_u32_e32 v2, 0x18c0, v0
	ds_write2_b32 v2, v30, v31 offset1:1
	v_add_u32_e32 v2, 0x18c8, v0
	ds_write2_b32 v2, v32, v33 offset1:1
	v_add_u32_e32 v2, 0x1ce0, v0
	v_add_u32_e32 v0, 0x1ce8, v0
	ds_write2_b32 v2, v26, v27 offset1:1
	ds_write2_b32 v0, v28, v29 offset1:1
	s_waitcnt lgkmcnt(0)
	v_lshl_add_u64 v[2:3], s[24:25], 1, v[42:43]
	v_cmp_gt_i32_e32 vcc, s30, v35
	s_and_saveexec_b64 s[4:5], vcc
	s_cbranch_execz .LBB0_194
	ds_read2_b32 v[4:5], v75 offset0:198 offset1:231
	ds_read2_b32 v[8:9], v75 offset0:132 offset1:165
	s_waitcnt lgkmcnt(1)
	v_cvt_pk_bf16_f32 v7, v4, v5
	ds_read2_b32 v[4:5], v75 offset0:66 offset1:99
	s_waitcnt lgkmcnt(1)
	v_cvt_pk_bf16_f32 v6, v8, v9
	ds_read2_b32 v[8:9], v75 offset1:33
	s_waitcnt lgkmcnt(1)
	v_cvt_pk_bf16_f32 v5, v4, v5
	s_waitcnt lgkmcnt(0)
	v_cvt_pk_bf16_f32 v4, v8, v9
	v_or_b32_e32 v8, s22, v35
	v_ashrrev_i32_e32 v9, 31, v8
	v_lshlrev_b64 v[8:9], 10, v[8:9]
	v_lshl_add_u64 v[8:9], v[2:3], 0, v[8:9]
	global_store_dwordx4 v[8:9], v[4:7], off
	s_or_b64 exec, exec, s[4:5]
	v_cmp_gt_i32_e32 vcc, s30, v69
	s_and_saveexec_b64 s[4:5], vcc
	s_cbranch_execnz .LBB0_195

; #define LAS __attribute__((address_space(3)))
; __device__ __forceinline__ unsigned pk2(float lo, float hi) { return f2bf(lo) | (f2bf(hi) << 16); }
; template <int MAPK>
; __device__ __forceinline__ void transpose_item(const float* W, int ldw, int k0, int n0, int ncnt, bf16* WT, int ldd, int dcol0, int moff, LAS float* scr, int lane, const float* gk) {
;     ...
;     const int c = lane & 7;
; #pragma unroll
;     for (int j = 0; j < 4; ++j) { const int n = (lane >> 3) + 8 * j; const LAS float* s = scr + (8 * c) * 33 + n;
;         v4u o; o.x = pk2(s[0 * 33], s[1 * 33]); o.y = pk2(s[2 * 33], s[3 * 33]); o.z = pk2(s[4 * 33], s[5 * 33]); o.w = pk2(s[6 * 33], s[7 * 33]);
;         const int sn = n0 + n - moff;
;         int drow;
;         if (MAPK == MAP_LIN) drow = sn; else if (MAPK == MAP_GATE) drow = 32 * (sn >> 4) + (sn & 15); else drow = 32 * (sn >> 4) + 16 + (sn & 15);
;         if (n < ncnt) *(v4u*)(WT + (size_t)drow * ldd + dcol0 + k0 + 8 * c) = o; }
.LBB0_193:
	ds_read2_b32 v[4:5], v75 offset0:214 offset1:247
	ds_read2_b32 v[8:9], v75 offset0:148 offset1:181
	s_waitcnt lgkmcnt(1)
	v_cvt_pk_bf16_f32 v7, v4, v5
	ds_read2_b32 v[4:5], v75 offset0:82 offset1:115
	s_waitcnt lgkmcnt(1)
	v_cvt_pk_bf16_f32 v6, v8, v9
	ds_read2_b32 v[8:9], v75 offset0:16 offset1:49
	s_waitcnt lgkmcnt(1)
	v_cvt_pk_bf16_f32 v5, v4, v5
	s_waitcnt lgkmcnt(0)
	v_cvt_pk_bf16_f32 v4, v8, v9
	v_or_b32_e32 v8, s22, v71
	v_ashrrev_i32_e32 v9, 31, v8
	v_lshlrev_b64 v[8:9], 10, v[8:9]
	v_lshl_add_u64 v[8:9], v[2:3], 0, v[8:9]
	global_store_dwordx4 v[8:9], v[4:7], off
	s_or_b64 exec, exec, s[4:5]
	v_cmp_gt_i32_e32 vcc, s30, v73
	s_and_saveexec_b64 s[4:5], vcc
	s_cbranch_execnz .LBB0_197
	s_branch .LBB0_198

; #define LAS __attribute__((address_space(3)))
; __device__ __forceinline__ unsigned pk2(float lo, float hi) { return f2bf(lo) | (f2bf(hi) << 16); }
; template <int MAPK>
; __device__ __forceinline__ void transpose_item(const float* W, int ldw, int k0, int n0, int ncnt, bf16* WT, int ldd, int dcol0, int moff, LAS float* scr, int lane, const float* gk) {
;     ...
;     const int c = lane & 7;
; #pragma unroll
;     for (int j = 0; j < 4; ++j) { const int n = (lane >> 3) + 8 * j; const LAS float* s = scr + (8 * c) * 33 + n;
;         v4u o; o.x = pk2(s[0 * 33], s[1 * 33]); o.y = pk2(s[2 * 33], s[3 * 33]); o.z = pk2(s[4 * 33], s[5 * 33]); o.w = pk2(s[6 * 33], s[7 * 33]);
;         const int sn = n0 + n - moff;
;         int drow;
;         if (MAPK == MAP_LIN) drow = sn; else if (MAPK == MAP_GATE) drow = 32 * (sn >> 4) + (sn & 15); else drow = 32 * (sn >> 4) + 16 + (sn & 15);
;         if (n < ncnt) *(v4u*)(WT + (size_t)drow * ldd + dcol0 + k0 + 8 * c) = o; }
.LBB0_195:
	ds_read2_b32 v[4:5], v75 offset0:206 offset1:239
	ds_read2_b32 v[8:9], v75 offset0:140 offset1:173
	s_waitcnt lgkmcnt(1)
	v_cvt_pk_bf16_f32 v7, v4, v5
	ds_read2_b32 v[4:5], v75 offset0:74 offset1:107
	s_waitcnt lgkmcnt(1)
	v_cvt_pk_bf16_f32 v6, v8, v9
	ds_read2_b32 v[8:9], v75 offset0:8 offset1:41
	s_waitcnt lgkmcnt(1)
	v_cvt_pk_bf16_f32 v5, v4, v5
	s_waitcnt lgkmcnt(0)
	v_cvt_pk_bf16_f32 v4, v8, v9
	v_or_b32_e32 v8, s22, v69
	v_ashrrev_i32_e32 v9, 31, v8
	v_lshlrev_b64 v[8:9], 10, v[8:9]
	v_lshl_add_u64 v[8:9], v[2:3], 0, v[8:9]
	global_store_dwordx4 v[8:9], v[4:7], off
	s_or_b64 exec, exec, s[4:5]
	v_cmp_gt_i32_e32 vcc, s30, v71
	s_and_saveexec_b64 s[4:5], vcc
	s_cbranch_execnz .LBB0_193

; #define LAS __attribute__((address_space(3)))
; __device__ __forceinline__ unsigned pk2(float lo, float hi) { return f2bf(lo) | (f2bf(hi) << 16); }
; template <int MAPK>
; __device__ __forceinline__ void transpose_item(const float* W, int ldw, int k0, int n0, int ncnt, bf16* WT, int ldd, int dcol0, int moff, LAS float* scr, int lane, const float* gk) {
;     ...
;     const int c = lane & 7;
; #pragma unroll
;     for (int j = 0; j < 4; ++j) { const int n = (lane >> 3) + 8 * j; const LAS float* s = scr + (8 * c) * 33 + n;
;         v4u o; o.x = pk2(s[0 * 33], s[1 * 33]); o.y = pk2(s[2 * 33], s[3 * 33]); o.z = pk2(s[4 * 33], s[5 * 33]); o.w = pk2(s[6 * 33], s[7 * 33]);
;         const int sn = n0 + n - moff;
;         int drow;
;         if (MAPK == MAP_LIN) drow = sn; else if (MAPK == MAP_GATE) drow = 32 * (sn >> 4) + (sn & 15); else drow = 32 * (sn >> 4) + 16 + (sn & 15);
;         if (n < ncnt) *(v4u*)(WT + (size_t)drow * ldd + dcol0 + k0 + 8 * c) = o; }
.LBB0_197:
	ds_read2_b32 v[4:5], v75 offset0:222 offset1:255
	ds_read2_b32 v[8:9], v75 offset0:156 offset1:189
	s_waitcnt lgkmcnt(1)
	v_cvt_pk_bf16_f32 v7, v4, v5
	ds_read2_b32 v[4:5], v75 offset0:90 offset1:123
	s_waitcnt lgkmcnt(1)
	v_cvt_pk_bf16_f32 v6, v8, v9
	ds_read2_b32 v[8:9], v75 offset0:24 offset1:57
	s_waitcnt lgkmcnt(1)
	v_cvt_pk_bf16_f32 v5, v4, v5
	s_waitcnt lgkmcnt(0)
	v_cvt_pk_bf16_f32 v4, v8, v9
	v_or_b32_e32 v8, s22, v73
	v_ashrrev_i32_e32 v9, 31, v8
	v_lshlrev_b64 v[8:9], 10, v[8:9]
	v_lshl_add_u64 v[2:3], v[2:3], 0, v[8:9]
	global_store_dwordx4 v[2:3], v[4:7], off

; #define LAS __attribute__((address_space(3)))
; #define LDS_WAIT() asm volatile("s_waitcnt lgkmcnt(0)" ::: "memory")
; __device__ __forceinline__ unsigned pk2(float lo, float hi) { return f2bf(lo) | (f2bf(hi) << 16); }
; template <int MAPK>
; __device__ __forceinline__ void transpose_item(const float* W, int ldw, int k0, int n0, int ncnt, bf16* WT, int ldd, int dcol0, int moff, LAS float* scr, int lane, const float* gk) {
;     ...
;       for (int j = 0; j < 8; ++j) { LAS float* d = scr + (8 * j + kr) * 33 + c4; d[0] = v[j].x; d[1] = v[j].y; d[2] = v[j].z; d[3] = v[j].w; } }
;     LDS_WAIT(); asm volatile("" ::: "memory");
;     const int c = lane & 7;
; #pragma unroll
;     for (int j = 0; j < 4; ++j) { const int n = (lane >> 3) + 8 * j; const LAS float* s = scr + (8 * c) * 33 + n;
;         v4u o; o.x = pk2(s[0 * 33], s[1 * 33]); o.y = pk2(s[2 * 33], s[3 * 33]); o.z = pk2(s[4 * 33], s[5 * 33]); o.w = pk2(s[6 * 33], s[7 * 33]);
;         const int sn = n0 + n - moff;
;         int drow;
;         if (MAPK == MAP_LIN) drow = sn; else if (MAPK == MAP_GATE) drow = 32 * (sn >> 4) + (sn & 15); else drow = 32 * (sn >> 4) + 16 + (sn & 15);
;         if (n < ncnt) *(v4u*)(WT + (size_t)drow * ldd + dcol0 + k0 + 8 * c) = o; }
.LBB0_219:
	s_or_b64 exec, exec, s[26:27]
	s_waitcnt vmcnt(0)
	v_add_u32_e32 v0, v37, v67
	v_add_u32_e32 v64, 0x420, v0
	s_ashr_i32 s25, s24, 31
	ds_write2_b32 v0, v2, v3 offset1:1
	ds_write2_b32 v0, v4, v5 offset0:2 offset1:3
	ds_write2_b32 v64, v6, v7 offset1:1
	v_add_u32_e32 v2, 0x428, v0
	ds_write2_b32 v2, v8, v9 offset1:1
	v_add_u32_e32 v2, 0x840, v0
	ds_write2_b32 v2, v14, v15 offset1:1
	v_add_u32_e32 v2, 0x848, v0
	ds_write2_b32 v2, v16, v17 offset1:1
	v_add_u32_e32 v2, 0xc60, v0
	ds_write2_b32 v2, v10, v11 offset1:1
	v_add_u32_e32 v2, 0xc68, v0
	ds_write2_b32 v2, v12, v13 offset1:1
	v_add_u32_e32 v2, 0x1080, v0
	ds_write2_b32 v2, v22, v23 offset1:1
	v_add_u32_e32 v2, 0x1088, v0
	ds_write2_b32 v2, v24, v25 offset1:1
	v_add_u32_e32 v2, 0x14a0, v0
	ds_write2_b32 v2, v18, v19 offset1:1
	v_add_u32_e32 v2, 0x14a8, v0
	ds_write2_b32 v2, v20, v21 offset1:1
	v_add_u32_e32 v2, 0x18c0, v0
	ds_write2_b32 v2, v30, v31 offset1:1
	v_add_u32_e32 v2, 0x18c8, v0
	ds_write2_b32 v2, v32, v33 offset1:1
	v_add_u32_e32 v2, 0x1ce0, v0
	v_add_u32_e32 v0, 0x1ce8, v0
	ds_write2_b32 v2, v26, v27 offset1:1
	ds_write2_b32 v0, v28, v29 offset1:1
	s_waitcnt lgkmcnt(0)
	v_lshl_add_u64 v[2:3], s[24:25], 1, v[44:45]
	v_cmp_gt_i32_e32 vcc, s31, v35
	s_and_saveexec_b64 s[4:5], vcc
	s_cbranch_execz .LBB0_223
	ds_read2_b32 v[4:5], v75 offset0:198 offset1:231
	ds_read2_b32 v[8:9], v75 offset0:132 offset1:165
	s_waitcnt lgkmcnt(1)
	v_cvt_pk_bf16_f32 v7, v4, v5
	ds_read2_b32 v[4:5], v75 offset0:66 offset1:99
	s_waitcnt lgkmcnt(1)
	v_cvt_pk_bf16_f32 v6, v8, v9
	ds_read2_b32 v[8:9], v75 offset1:33
	s_waitcnt lgkmcnt(1)
	v_cvt_pk_bf16_f32 v5, v4, v5
	s_waitcnt lgkmcnt(0)
	v_cvt_pk_bf16_f32 v4, v8, v9
	v_or_b32_e32 v8, s22, v35
	v_ashrrev_i32_e32 v9, 31, v8
	v_lshlrev_b64 v[8:9], 10, v[8:9]
	v_lshl_add_u64 v[8:9], v[2:3], 0, v[8:9]
	global_store_dwordx4 v[8:9], v[4:7], off
	s_or_b64 exec, exec, s[4:5]
	v_cmp_gt_i32_e32 vcc, s31, v69
	s_and_saveexec_b64 s[4:5], vcc
	s_cbranch_execnz .LBB0_224

; #define LAS __attribute__((address_space(3)))
; __device__ __forceinline__ unsigned pk2(float lo, float hi) { return f2bf(lo) | (f2bf(hi) << 16); }
; template <int MAPK>
; __device__ __forceinline__ void transpose_item(const float* W, int ldw, int k0, int n0, int ncnt, bf16* WT, int ldd, int dcol0, int moff, LAS float* scr, int lane, const float* gk) {
;     ...
;     const int c = lane & 7;
; #pragma unroll
;     for (int j = 0; j < 4; ++j) { const int n = (lane >> 3) + 8 * j; const LAS float* s = scr + (8 * c) * 33 + n;
;         v4u o; o.x = pk2(s[0 * 33], s[1 * 33]); o.y = pk2(s[2 * 33], s[3 * 33]); o.z = pk2(s[4 * 33], s[5 * 33]); o.w = pk2(s[6 * 33], s[7 * 33]);
;         const int sn = n0 + n - moff;
;         int drow;
;         if (MAPK == MAP_LIN) drow = sn; else if (MAPK == MAP_GATE) drow = 32 * (sn >> 4) + (sn & 15); else drow = 32 * (sn >> 4) + 16 + (sn & 15);
;         if (n < ncnt) *(v4u*)(WT + (size_t)drow * ldd + dcol0 + k0 + 8 * c) = o; }
.LBB0_222:
	ds_read2_b32 v[4:5], v75 offset0:214 offset1:247
	ds_read2_b32 v[8:9], v75 offset0:148 offset1:181
	s_waitcnt lgkmcnt(1)
	v_cvt_pk_bf16_f32 v7, v4, v5
	ds_read2_b32 v[4:5], v75 offset0:82 offset1:115
	s_waitcnt lgkmcnt(1)
	v_cvt_pk_bf16_f32 v6, v8, v9
	ds_read2_b32 v[8:9], v75 offset0:16 offset1:49
	s_waitcnt lgkmcnt(1)
	v_cvt_pk_bf16_f32 v5, v4, v5
	s_waitcnt lgkmcnt(0)
	v_cvt_pk_bf16_f32 v4, v8, v9
	v_or_b32_e32 v8, s22, v71
	v_ashrrev_i32_e32 v9, 31, v8
	v_lshlrev_b64 v[8:9], 10, v[8:9]
	v_lshl_add_u64 v[8:9], v[2:3], 0, v[8:9]
	global_store_dwordx4 v[8:9], v[4:7], off
	s_or_b64 exec, exec, s[4:5]
	v_cmp_gt_i32_e32 vcc, s31, v73
	s_and_saveexec_b64 s[4:5], vcc
	s_cbranch_execnz .LBB0_226
	s_branch .LBB0_227

; #define LAS __attribute__((address_space(3)))
; __device__ __forceinline__ unsigned pk2(float lo, float hi) { return f2bf(lo) | (f2bf(hi) << 16); }
; template <int MAPK>
; __device__ __forceinline__ void transpose_item(const float* W, int ldw, int k0, int n0, int ncnt, bf16* WT, int ldd, int dcol0, int moff, LAS float* scr, int lane, const float* gk) {
;     ...
;     const int c = lane & 7;
; #pragma unroll
;     for (int j = 0; j < 4; ++j) { const int n = (lane >> 3) + 8 * j; const LAS float* s = scr + (8 * c) * 33 + n;
;         v4u o; o.x = pk2(s[0 * 33], s[1 * 33]); o.y = pk2(s[2 * 33], s[3 * 33]); o.z = pk2(s[4 * 33], s[5 * 33]); o.w = pk2(s[6 * 33], s[7 * 33]);
;         const int sn = n0 + n - moff;
;         int drow;
;         if (MAPK == MAP_LIN) drow = sn; else if (MAPK == MAP_GATE) drow = 32 * (sn >> 4) + (sn & 15); else drow = 32 * (sn >> 4) + 16 + (sn & 15);
;         if (n < ncnt) *(v4u*)(WT + (size_t)drow * ldd + dcol0 + k0 + 8 * c) = o; }
.LBB0_224:
	ds_read2_b32 v[4:5], v75 offset0:206 offset1:239
	ds_read2_b32 v[8:9], v75 offset0:140 offset1:173
	s_waitcnt lgkmcnt(1)
	v_cvt_pk_bf16_f32 v7, v4, v5
	ds_read2_b32 v[4:5], v75 offset0:74 offset1:107
	s_waitcnt lgkmcnt(1)
	v_cvt_pk_bf16_f32 v6, v8, v9
	ds_read2_b32 v[8:9], v75 offset0:8 offset1:41
	s_waitcnt lgkmcnt(1)
	v_cvt_pk_bf16_f32 v5, v4, v5
	s_waitcnt lgkmcnt(0)
	v_cvt_pk_bf16_f32 v4, v8, v9
	v_or_b32_e32 v8, s22, v69
	v_ashrrev_i32_e32 v9, 31, v8
	v_lshlrev_b64 v[8:9], 10, v[8:9]
	v_lshl_add_u64 v[8:9], v[2:3], 0, v[8:9]
	global_store_dwordx4 v[8:9], v[4:7], off
	s_or_b64 exec, exec, s[4:5]
	v_cmp_gt_i32_e32 vcc, s31, v71
	s_and_saveexec_b64 s[4:5], vcc
	s_cbranch_execnz .LBB0_222

; #define LAS __attribute__((address_space(3)))
; #define LDS_WAIT() asm volatile("s_waitcnt lgkmcnt(0)" ::: "memory")
; __device__ __forceinline__ unsigned pk2(float lo, float hi) { return f2bf(lo) | (f2bf(hi) << 16); }
; template <int MAPK>
; __device__ __forceinline__ void transpose_item(const float* W, int ldw, int k0, int n0, int ncnt, bf16* WT, int ldd, int dcol0, int moff, LAS float* scr, int lane, const float* gk) {
;     ...
;       for (int j = 0; j < 8; ++j) { LAS float* d = scr + (8 * j + kr) * 33 + c4; d[0] = v[j].x; d[1] = v[j].y; d[2] = v[j].z; d[3] = v[j].w; } }
;     LDS_WAIT(); asm volatile("" ::: "memory");
;     const int c = lane & 7;
; #pragma unroll
;     for (int j = 0; j < 4; ++j) { const int n = (lane >> 3) + 8 * j; const LAS float* s = scr + (8 * c) * 33 + n;
;         v4u o; o.x = pk2(s[0 * 33], s[1 * 33]); o.y = pk2(s[2 * 33], s[3 * 33]); o.z = pk2(s[4 * 33], s[5 * 33]); o.w = pk2(s[6 * 33], s[7 * 33]);
;         const int sn = n0 + n - moff;
;         int drow;
;         if (MAPK == MAP_LIN) drow = sn; else if (MAPK == MAP_GATE) drow = 32 * (sn >> 4) + (sn & 15); else drow = 32 * (sn >> 4) + 16 + (sn & 15);
;         if (n < ncnt) *(v4u*)(WT + (size_t)drow * ldd + dcol0 + k0 + 8 * c) = o; }
.LBB0_248:
	s_or_b64 exec, exec, s[26:27]
	s_waitcnt vmcnt(0)
	v_add_u32_e32 v0, v37, v67
	v_add_u32_e32 v64, 0x420, v0
	s_ashr_i32 s25, s24, 31
	ds_write2_b32 v0, v2, v3 offset1:1
	ds_write2_b32 v0, v4, v5 offset0:2 offset1:3
	ds_write2_b32 v64, v6, v7 offset1:1
	v_add_u32_e32 v2, 0x428, v0
	ds_write2_b32 v2, v8, v9 offset1:1
	v_add_u32_e32 v2, 0x840, v0
	ds_write2_b32 v2, v14, v15 offset1:1
	v_add_u32_e32 v2, 0x848, v0
	ds_write2_b32 v2, v16, v17 offset1:1
	v_add_u32_e32 v2, 0xc60, v0
	ds_write2_b32 v2, v10, v11 offset1:1
	v_add_u32_e32 v2, 0xc68, v0
	ds_write2_b32 v2, v12, v13 offset1:1
	v_add_u32_e32 v2, 0x1080, v0
	ds_write2_b32 v2, v22, v23 offset1:1
	v_add_u32_e32 v2, 0x1088, v0
	ds_write2_b32 v2, v24, v25 offset1:1
	v_add_u32_e32 v2, 0x14a0, v0
	ds_write2_b32 v2, v18, v19 offset1:1
	v_add_u32_e32 v2, 0x14a8, v0
	ds_write2_b32 v2, v20, v21 offset1:1
	v_add_u32_e32 v2, 0x18c0, v0
	ds_write2_b32 v2, v30, v31 offset1:1
	v_add_u32_e32 v2, 0x18c8, v0
	ds_write2_b32 v2, v32, v33 offset1:1
	v_add_u32_e32 v2, 0x1ce0, v0
	v_add_u32_e32 v0, 0x1ce8, v0
	ds_write2_b32 v2, v26, v27 offset1:1
	ds_write2_b32 v0, v28, v29 offset1:1
	s_waitcnt lgkmcnt(0)
	v_lshl_add_u64 v[2:3], s[24:25], 1, v[46:47]
	v_cmp_gt_i32_e32 vcc, s30, v35
	s_and_saveexec_b64 s[4:5], vcc
	s_cbranch_execz .LBB0_252
	ds_read2_b32 v[4:5], v75 offset0:198 offset1:231
	ds_read2_b32 v[8:9], v75 offset0:132 offset1:165
	s_movk_i32 s23, 0x1800
	s_waitcnt lgkmcnt(1)
	v_cvt_pk_bf16_f32 v7, v4, v5
	ds_read2_b32 v[4:5], v75 offset0:66 offset1:99
	s_waitcnt lgkmcnt(1)
	v_cvt_pk_bf16_f32 v6, v8, v9
	ds_read2_b32 v[8:9], v75 offset1:33
	s_waitcnt lgkmcnt(1)
	v_cvt_pk_bf16_f32 v5, v4, v5
	s_waitcnt lgkmcnt(0)
	v_cvt_pk_bf16_f32 v4, v8, v9
	v_or_b32_e32 v0, s22, v35
	v_mad_i64_i32 v[8:9], s[24:25], v0, s23, v[2:3]
	global_store_dwordx4 v[8:9], v[4:7], off
	s_or_b64 exec, exec, s[4:5]
	v_cmp_gt_i32_e32 vcc, s30, v69
	s_and_saveexec_b64 s[4:5], vcc
	s_cbranch_execnz .LBB0_253

; #define LAS __attribute__((address_space(3)))
; __device__ __forceinline__ unsigned pk2(float lo, float hi) { return f2bf(lo) | (f2bf(hi) << 16); }
; template <int MAPK>
; __device__ __forceinline__ void transpose_item(const float* W, int ldw, int k0, int n0, int ncnt, bf16* WT, int ldd, int dcol0, int moff, LAS float* scr, int lane, const float* gk) {
;     ...
;     const int c = lane & 7;
; #pragma unroll
;     for (int j = 0; j < 4; ++j) { const int n = (lane >> 3) + 8 * j; const LAS float* s = scr + (8 * c) * 33 + n;
;         v4u o; o.x = pk2(s[0 * 33], s[1 * 33]); o.y = pk2(s[2 * 33], s[3 * 33]); o.z = pk2(s[4 * 33], s[5 * 33]); o.w = pk2(s[6 * 33], s[7 * 33]);
;         const int sn = n0 + n - moff;
;         int drow;
;         if (MAPK == MAP_LIN) drow = sn; else if (MAPK == MAP_GATE) drow = 32 * (sn >> 4) + (sn & 15); else drow = 32 * (sn >> 4) + 16 + (sn & 15);
;         if (n < ncnt) *(v4u*)(WT + (size_t)drow * ldd + dcol0 + k0 + 8 * c) = o; }
.LBB0_251:
	ds_read2_b32 v[4:5], v75 offset0:214 offset1:247
	ds_read2_b32 v[8:9], v75 offset0:148 offset1:181
	s_movk_i32 s23, 0x1800
	s_waitcnt lgkmcnt(1)
	v_cvt_pk_bf16_f32 v7, v4, v5
	ds_read2_b32 v[4:5], v75 offset0:82 offset1:115
	s_waitcnt lgkmcnt(1)
	v_cvt_pk_bf16_f32 v6, v8, v9
	ds_read2_b32 v[8:9], v75 offset0:16 offset1:49
	s_waitcnt lgkmcnt(1)
	v_cvt_pk_bf16_f32 v5, v4, v5
	s_waitcnt lgkmcnt(0)
	v_cvt_pk_bf16_f32 v4, v8, v9
	v_or_b32_e32 v0, s22, v71
	v_mad_i64_i32 v[8:9], s[24:25], v0, s23, v[2:3]
	global_store_dwordx4 v[8:9], v[4:7], off
	s_or_b64 exec, exec, s[4:5]
	v_cmp_gt_i32_e32 vcc, s30, v73
	s_and_saveexec_b64 s[4:5], vcc
	s_cbranch_execnz .LBB0_255
	s_branch .LBB0_256

; #define LAS __attribute__((address_space(3)))
; __device__ __forceinline__ unsigned pk2(float lo, float hi) { return f2bf(lo) | (f2bf(hi) << 16); }
; template <int MAPK>
; __device__ __forceinline__ void transpose_item(const float* W, int ldw, int k0, int n0, int ncnt, bf16* WT, int ldd, int dcol0, int moff, LAS float* scr, int lane, const float* gk) {
;     ...
;     const int c = lane & 7;
; #pragma unroll
;     for (int j = 0; j < 4; ++j) { const int n = (lane >> 3) + 8 * j; const LAS float* s = scr + (8 * c) * 33 + n;
;         v4u o; o.x = pk2(s[0 * 33], s[1 * 33]); o.y = pk2(s[2 * 33], s[3 * 33]); o.z = pk2(s[4 * 33], s[5 * 33]); o.w = pk2(s[6 * 33], s[7 * 33]);
;         const int sn = n0 + n - moff;
;         int drow;
;         if (MAPK == MAP_LIN) drow = sn; else if (MAPK == MAP_GATE) drow = 32 * (sn >> 4) + (sn & 15); else drow = 32 * (sn >> 4) + 16 + (sn & 15);
;         if (n < ncnt) *(v4u*)(WT + (size_t)drow * ldd + dcol0 + k0 + 8 * c) = o; }
.LBB0_253:
	ds_read2_b32 v[4:5], v75 offset0:206 offset1:239
	ds_read2_b32 v[8:9], v75 offset0:140 offset1:173
	s_movk_i32 s23, 0x1800
	s_waitcnt lgkmcnt(1)
	v_cvt_pk_bf16_f32 v7, v4, v5
	ds_read2_b32 v[4:5], v75 offset0:74 offset1:107
	s_waitcnt lgkmcnt(1)
	v_cvt_pk_bf16_f32 v6, v8, v9
	ds_read2_b32 v[8:9], v75 offset0:8 offset1:41
	s_waitcnt lgkmcnt(1)
	v_cvt_pk_bf16_f32 v5, v4, v5
	s_waitcnt lgkmcnt(0)
	v_cvt_pk_bf16_f32 v4, v8, v9
	v_or_b32_e32 v0, s22, v69
	v_mad_i64_i32 v[8:9], s[24:25], v0, s23, v[2:3]
	global_store_dwordx4 v[8:9], v[4:7], off
	s_or_b64 exec, exec, s[4:5]
	v_cmp_gt_i32_e32 vcc, s30, v71
	s_and_saveexec_b64 s[4:5], vcc
	s_cbranch_execnz .LBB0_251

; #define LAS __attribute__((address_space(3)))
; __device__ __forceinline__ unsigned pk2(float lo, float hi) { return f2bf(lo) | (f2bf(hi) << 16); }
; template <int MAPK>
; __device__ __forceinline__ void transpose_item(const float* W, int ldw, int k0, int n0, int ncnt, bf16* WT, int ldd, int dcol0, int moff, LAS float* scr, int lane, const float* gk) {
;     ...
;     const int c = lane & 7;
; #pragma unroll
;     for (int j = 0; j < 4; ++j) { const int n = (lane >> 3) + 8 * j; const LAS float* s = scr + (8 * c) * 33 + n;
;         v4u o; o.x = pk2(s[0 * 33], s[1 * 33]); o.y = pk2(s[2 * 33], s[3 * 33]); o.z = pk2(s[4 * 33], s[5 * 33]); o.w = pk2(s[6 * 33], s[7 * 33]);
;         const int sn = n0 + n - moff;
;         int drow;
;         if (MAPK == MAP_LIN) drow = sn; else if (MAPK == MAP_GATE) drow = 32 * (sn >> 4) + (sn & 15); else drow = 32 * (sn >> 4) + 16 + (sn & 15);
;         if (n < ncnt) *(v4u*)(WT + (size_t)drow * ldd + dcol0 + k0 + 8 * c) = o; }
.LBB0_255:
	ds_read2_b32 v[4:5], v75 offset0:222 offset1:255
	ds_read2_b32 v[8:9], v75 offset0:156 offset1:189
	s_waitcnt lgkmcnt(1)
	v_cvt_pk_bf16_f32 v7, v4, v5
	ds_read2_b32 v[4:5], v75 offset0:90 offset1:123
	s_waitcnt lgkmcnt(1)
	v_cvt_pk_bf16_f32 v6, v8, v9
	ds_read2_b32 v[8:9], v75 offset0:24 offset1:57
	s_waitcnt lgkmcnt(1)
	v_cvt_pk_bf16_f32 v5, v4, v5
	s_waitcnt lgkmcnt(0)
	v_cvt_pk_bf16_f32 v4, v8, v9
	v_or_b32_e32 v0, s22, v73
	s_movk_i32 s22, 0x1800
	v_mad_i64_i32 v[2:3], s[22:23], v0, s22, v[2:3]
	global_store_dwordx4 v[2:3], v[4:7], off

; #define LAS __attribute__((address_space(3)))
; #define LDS_WAIT() asm volatile("s_waitcnt lgkmcnt(0)" ::: "memory")
; __device__ __forceinline__ unsigned pk2(float lo, float hi) { return f2bf(lo) | (f2bf(hi) << 16); }
; template <int MAPK>
; __device__ __forceinline__ void transpose_item(const float* W, int ldw, int k0, int n0, int ncnt, bf16* WT, int ldd, int dcol0, int moff, LAS float* scr, int lane, const float* gk) {
;     ...
;       for (int j = 0; j < 8; ++j) { LAS float* d = scr + (8 * j + kr) * 33 + c4; d[0] = v[j].x; d[1] = v[j].y; d[2] = v[j].z; d[3] = v[j].w; } }
;     LDS_WAIT(); asm volatile("" ::: "memory");
;     const int c = lane & 7;
; #pragma unroll
;     for (int j = 0; j < 4; ++j) { const int n = (lane >> 3) + 8 * j; const LAS float* s = scr + (8 * c) * 33 + n;
;         v4u o; o.x = pk2(s[0 * 33], s[1 * 33]); o.y = pk2(s[2 * 33], s[3 * 33]); o.z = pk2(s[4 * 33], s[5 * 33]); o.w = pk2(s[6 * 33], s[7 * 33]);
;         const int sn = n0 + n - moff;
;         int drow;
;         if (MAPK == MAP_LIN) drow = sn; else if (MAPK == MAP_GATE) drow = 32 * (sn >> 4) + (sn & 15); else drow = 32 * (sn >> 4) + 16 + (sn & 15);
;         if (n < ncnt) *(v4u*)(WT + (size_t)drow * ldd + dcol0 + k0 + 8 * c) = o; }
.LBB0_277:
	s_or_b64 exec, exec, s[26:27]
	s_waitcnt vmcnt(0)
	v_add_u32_e32 v0, v37, v67
	v_add_u32_e32 v64, 0x420, v0
	s_ashr_i32 s25, s24, 31
	ds_write2_b32 v0, v2, v3 offset1:1
	ds_write2_b32 v0, v4, v5 offset0:2 offset1:3
	ds_write2_b32 v64, v6, v7 offset1:1
	v_add_u32_e32 v2, 0x428, v0
	ds_write2_b32 v2, v8, v9 offset1:1
	v_add_u32_e32 v2, 0x840, v0
	ds_write2_b32 v2, v14, v15 offset1:1
	v_add_u32_e32 v2, 0x848, v0
	ds_write2_b32 v2, v16, v17 offset1:1
	v_add_u32_e32 v2, 0xc60, v0
	ds_write2_b32 v2, v10, v11 offset1:1
	v_add_u32_e32 v2, 0xc68, v0
	ds_write2_b32 v2, v12, v13 offset1:1
	v_add_u32_e32 v2, 0x1080, v0
	ds_write2_b32 v2, v22, v23 offset1:1
	v_add_u32_e32 v2, 0x1088, v0
	ds_write2_b32 v2, v24, v25 offset1:1
	v_add_u32_e32 v2, 0x14a0, v0
	ds_write2_b32 v2, v18, v19 offset1:1
	v_add_u32_e32 v2, 0x14a8, v0
	ds_write2_b32 v2, v20, v21 offset1:1
	v_add_u32_e32 v2, 0x18c0, v0
	ds_write2_b32 v2, v30, v31 offset1:1
	v_add_u32_e32 v2, 0x18c8, v0
	ds_write2_b32 v2, v32, v33 offset1:1
	v_add_u32_e32 v2, 0x1ce0, v0
	v_add_u32_e32 v0, 0x1ce8, v0
	ds_write2_b32 v2, v26, v27 offset1:1
	ds_write2_b32 v0, v28, v29 offset1:1
	s_waitcnt lgkmcnt(0)
	v_lshl_add_u64 v[2:3], s[24:25], 1, v[48:49]
	v_cmp_gt_i32_e32 vcc, s31, v35
	s_and_saveexec_b64 s[4:5], vcc
	s_cbranch_execz .LBB0_281
	ds_read2_b32 v[4:5], v75 offset0:198 offset1:231
	ds_read2_b32 v[8:9], v75 offset0:132 offset1:165
	s_movk_i32 s23, 0x1800
	s_waitcnt lgkmcnt(1)
	v_cvt_pk_bf16_f32 v7, v4, v5
	ds_read2_b32 v[4:5], v75 offset0:66 offset1:99
	s_waitcnt lgkmcnt(1)
	v_cvt_pk_bf16_f32 v6, v8, v9
	ds_read2_b32 v[8:9], v75 offset1:33
	s_waitcnt lgkmcnt(1)
	v_cvt_pk_bf16_f32 v5, v4, v5
	s_waitcnt lgkmcnt(0)
	v_cvt_pk_bf16_f32 v4, v8, v9
	v_or_b32_e32 v0, s22, v35
	v_mad_i64_i32 v[8:9], s[24:25], v0, s23, v[2:3]
	global_store_dwordx4 v[8:9], v[4:7], off
	s_or_b64 exec, exec, s[4:5]
	v_cmp_gt_i32_e32 vcc, s31, v69
	s_and_saveexec_b64 s[4:5], vcc
	s_cbranch_execnz .LBB0_282

; #define LAS __attribute__((address_space(3)))
; __device__ __forceinline__ unsigned pk2(float lo, float hi) { return f2bf(lo) | (f2bf(hi) << 16); }
; template <int MAPK>
; __device__ __forceinline__ void transpose_item(const float* W, int ldw, int k0, int n0, int ncnt, bf16* WT, int ldd, int dcol0, int moff, LAS float* scr, int lane, const float* gk) {
;     ...
;     const int c = lane & 7;
; #pragma unroll
;     for (int j = 0; j < 4; ++j) { const int n = (lane >> 3) + 8 * j; const LAS float* s = scr + (8 * c) * 33 + n;
;         v4u o; o.x = pk2(s[0 * 33], s[1 * 33]); o.y = pk2(s[2 * 33], s[3 * 33]); o.z = pk2(s[4 * 33], s[5 * 33]); o.w = pk2(s[6 * 33], s[7 * 33]);
;         const int sn = n0 + n - moff;
;         int drow;
;         if (MAPK == MAP_LIN) drow = sn; else if (MAPK == MAP_GATE) drow = 32 * (sn >> 4) + (sn & 15); else drow = 32 * (sn >> 4) + 16 + (sn & 15);
;         if (n < ncnt) *(v4u*)(WT + (size_t)drow * ldd + dcol0 + k0 + 8 * c) = o; }
.LBB0_280:
	ds_read2_b32 v[4:5], v75 offset0:214 offset1:247
	ds_read2_b32 v[8:9], v75 offset0:148 offset1:181
	s_movk_i32 s23, 0x1800
	s_waitcnt lgkmcnt(1)
	v_cvt_pk_bf16_f32 v7, v4, v5
	ds_read2_b32 v[4:5], v75 offset0:82 offset1:115
	s_waitcnt lgkmcnt(1)
	v_cvt_pk_bf16_f32 v6, v8, v9
	ds_read2_b32 v[8:9], v75 offset0:16 offset1:49
	s_waitcnt lgkmcnt(1)
	v_cvt_pk_bf16_f32 v5, v4, v5
	s_waitcnt lgkmcnt(0)
	v_cvt_pk_bf16_f32 v4, v8, v9
	v_or_b32_e32 v0, s22, v71
	v_mad_i64_i32 v[8:9], s[24:25], v0, s23, v[2:3]
	global_store_dwordx4 v[8:9], v[4:7], off
	s_or_b64 exec, exec, s[4:5]
	v_cmp_gt_i32_e32 vcc, s31, v73
	s_and_saveexec_b64 s[4:5], vcc
	s_cbranch_execnz .LBB0_284
	s_branch .LBB0_285

; #define LAS __attribute__((address_space(3)))
; __device__ __forceinline__ unsigned pk2(float lo, float hi) { return f2bf(lo) | (f2bf(hi) << 16); }
; template <int MAPK>
; __device__ __forceinline__ void transpose_item(const float* W, int ldw, int k0, int n0, int ncnt, bf16* WT, int ldd, int dcol0, int moff, LAS float* scr, int lane, const float* gk) {
;     ...
;     const int c = lane & 7;
; #pragma unroll
;     for (int j = 0; j < 4; ++j) { const int n = (lane >> 3) + 8 * j; const LAS float* s = scr + (8 * c) * 33 + n;
;         v4u o; o.x = pk2(s[0 * 33], s[1 * 33]); o.y = pk2(s[2 * 33], s[3 * 33]); o.z = pk2(s[4 * 33], s[5 * 33]); o.w = pk2(s[6 * 33], s[7 * 33]);
;         const int sn = n0 + n - moff;
;         int drow;
;         if (MAPK == MAP_LIN) drow = sn; else if (MAPK == MAP_GATE) drow = 32 * (sn >> 4) + (sn & 15); else drow = 32 * (sn >> 4) + 16 + (sn & 15);
;         if (n < ncnt) *(v4u*)(WT + (size_t)drow * ldd + dcol0 + k0 + 8 * c) = o; }
.LBB0_282:
	ds_read2_b32 v[4:5], v75 offset0:206 offset1:239
	ds_read2_b32 v[8:9], v75 offset0:140 offset1:173
	s_movk_i32 s23, 0x1800
	s_waitcnt lgkmcnt(1)
	v_cvt_pk_bf16_f32 v7, v4, v5
	ds_read2_b32 v[4:5], v75 offset0:74 offset1:107
	s_waitcnt lgkmcnt(1)
	v_cvt_pk_bf16_f32 v6, v8, v9
	ds_read2_b32 v[8:9], v75 offset0:8 offset1:41
	s_waitcnt lgkmcnt(1)
	v_cvt_pk_bf16_f32 v5, v4, v5
	s_waitcnt lgkmcnt(0)
	v_cvt_pk_bf16_f32 v4, v8, v9
	v_or_b32_e32 v0, s22, v69
	v_mad_i64_i32 v[8:9], s[24:25], v0, s23, v[2:3]
	global_store_dwordx4 v[8:9], v[4:7], off
	s_or_b64 exec, exec, s[4:5]
	v_cmp_gt_i32_e32 vcc, s31, v71
	s_and_saveexec_b64 s[4:5], vcc
	s_cbranch_execnz .LBB0_280

; #define LAS __attribute__((address_space(3)))
; #define LDS_WAIT() asm volatile("s_waitcnt lgkmcnt(0)" ::: "memory")
; __device__ __forceinline__ unsigned pk2(float lo, float hi) { return f2bf(lo) | (f2bf(hi) << 16); }
; template <int MAPK>
; __device__ __forceinline__ void transpose_item(const float* W, int ldw, int k0, int n0, int ncnt, bf16* WT, int ldd, int dcol0, int moff, LAS float* scr, int lane, const float* gk) {
;     ...
;       for (int j = 0; j < 8; ++j) { LAS float* d = scr + (8 * j + kr) * 33 + c4; d[0] = v[j].x; d[1] = v[j].y; d[2] = v[j].z; d[3] = v[j].w; } }
;     LDS_WAIT(); asm volatile("" ::: "memory");
;     const int c = lane & 7;
; #pragma unroll
;     for (int j = 0; j < 4; ++j) { const int n = (lane >> 3) + 8 * j; const LAS float* s = scr + (8 * c) * 33 + n;
;         v4u o; o.x = pk2(s[0 * 33], s[1 * 33]); o.y = pk2(s[2 * 33], s[3 * 33]); o.z = pk2(s[4 * 33], s[5 * 33]); o.w = pk2(s[6 * 33], s[7 * 33]);
;         const int sn = n0 + n - moff;
;         int drow;
;         if (MAPK == MAP_LIN) drow = sn; else if (MAPK == MAP_GATE) drow = 32 * (sn >> 4) + (sn & 15); else drow = 32 * (sn >> 4) + 16 + (sn & 15);
;         if (n < ncnt) *(v4u*)(WT + (size_t)drow * ldd + dcol0 + k0 + 8 * c) = o; }
.LBB0_306:
	s_or_b64 exec, exec, s[26:27]
	s_waitcnt vmcnt(0)
	v_add_u32_e32 v0, v37, v67
	v_add_u32_e32 v64, 0x420, v0
	s_ashr_i32 s25, s24, 31
	ds_write2_b32 v0, v2, v3 offset1:1
	ds_write2_b32 v0, v4, v5 offset0:2 offset1:3
	ds_write2_b32 v64, v6, v7 offset1:1
	v_add_u32_e32 v2, 0x428, v0
	ds_write2_b32 v2, v8, v9 offset1:1
	v_add_u32_e32 v2, 0x840, v0
	ds_write2_b32 v2, v14, v15 offset1:1
	v_add_u32_e32 v2, 0x848, v0
	ds_write2_b32 v2, v16, v17 offset1:1
	v_add_u32_e32 v2, 0xc60, v0
	ds_write2_b32 v2, v10, v11 offset1:1
	v_add_u32_e32 v2, 0xc68, v0
	ds_write2_b32 v2, v12, v13 offset1:1
	v_add_u32_e32 v2, 0x1080, v0
	ds_write2_b32 v2, v22, v23 offset1:1
	v_add_u32_e32 v2, 0x1088, v0
	ds_write2_b32 v2, v24, v25 offset1:1
	v_add_u32_e32 v2, 0x14a0, v0
	ds_write2_b32 v2, v18, v19 offset1:1
	v_add_u32_e32 v2, 0x14a8, v0
	ds_write2_b32 v2, v20, v21 offset1:1
	v_add_u32_e32 v2, 0x18c0, v0
	ds_write2_b32 v2, v30, v31 offset1:1
	v_add_u32_e32 v2, 0x18c8, v0
	ds_write2_b32 v2, v32, v33 offset1:1
	v_add_u32_e32 v2, 0x1ce0, v0
	v_add_u32_e32 v0, 0x1ce8, v0
	ds_write2_b32 v2, v26, v27 offset1:1
	ds_write2_b32 v0, v28, v29 offset1:1
	s_waitcnt lgkmcnt(0)
	v_lshl_add_u64 v[2:3], s[24:25], 1, v[50:51]
	v_cmp_gt_i32_e32 vcc, s30, v35
	s_and_saveexec_b64 s[4:5], vcc
	s_cbranch_execz .LBB0_310
	ds_read2_b32 v[4:5], v75 offset0:198 offset1:231
	ds_read2_b32 v[8:9], v75 offset0:132 offset1:165
	s_movk_i32 s23, 0x1800
	s_waitcnt lgkmcnt(1)
	v_cvt_pk_bf16_f32 v7, v4, v5
	ds_read2_b32 v[4:5], v75 offset0:66 offset1:99
	s_waitcnt lgkmcnt(1)
	v_cvt_pk_bf16_f32 v6, v8, v9
	ds_read2_b32 v[8:9], v75 offset1:33
	s_waitcnt lgkmcnt(1)
	v_cvt_pk_bf16_f32 v5, v4, v5
	s_waitcnt lgkmcnt(0)
	v_cvt_pk_bf16_f32 v4, v8, v9
	v_or_b32_e32 v0, s22, v35
	v_mad_i64_i32 v[8:9], s[24:25], v0, s23, v[2:3]
	global_store_dwordx4 v[8:9], v[4:7], off
	s_or_b64 exec, exec, s[4:5]
	v_cmp_gt_i32_e32 vcc, s30, v69
	s_and_saveexec_b64 s[4:5], vcc
	s_cbranch_execnz .LBB0_311

; #define LAS __attribute__((address_space(3)))
; #define LDS_WAIT() asm volatile("s_waitcnt lgkmcnt(0)" ::: "memory")
; __device__ __forceinline__ unsigned pk2(float lo, float hi) { return f2bf(lo) | (f2bf(hi) << 16); }
; template <int MAPK>
; __device__ __forceinline__ void transpose_item(const float* W, int ldw, int k0, int n0, int ncnt, bf16* WT, int ldd, int dcol0, int moff, LAS float* scr, int lane, const float* gk) {
;     ...
;       for (int j = 0; j < 8; ++j) { LAS float* d = scr + (8 * j + kr) * 33 + c4; d[0] = v[j].x; d[1] = v[j].y; d[2] = v[j].z; d[3] = v[j].w; } }
;     LDS_WAIT(); asm volatile("" ::: "memory");
;     const int c = lane & 7;
; #pragma unroll
;     for (int j = 0; j < 4; ++j) { const int n = (lane >> 3) + 8 * j; const LAS float* s = scr + (8 * c) * 33 + n;
;         v4u o; o.x = pk2(s[0 * 33], s[1 * 33]); o.y = pk2(s[2 * 33], s[3 * 33]); o.z = pk2(s[4 * 33], s[5 * 33]); o.w = pk2(s[6 * 33], s[7 * 33]);
;         const int sn = n0 + n - moff;
;         int drow;
;         if (MAPK == MAP_LIN) drow = sn; else if (MAPK == MAP_GATE) drow = 32 * (sn >> 4) + (sn & 15); else drow = 32 * (sn >> 4) + 16 + (sn & 15);
;         if (n < ncnt) *(v4u*)(WT + (size_t)drow * ldd + dcol0 + k0 + 8 * c) = o; }
.LBB0_335:
	s_or_b64 exec, exec, s[26:27]
	s_waitcnt vmcnt(0)
	v_add_u32_e32 v0, v37, v67
	v_add_u32_e32 v64, 0x420, v0
	s_ashr_i32 s25, s24, 31
	ds_write2_b32 v0, v2, v3 offset1:1
	ds_write2_b32 v0, v4, v5 offset0:2 offset1:3
	ds_write2_b32 v64, v6, v7 offset1:1
	v_add_u32_e32 v2, 0x428, v0
	ds_write2_b32 v2, v8, v9 offset1:1
	v_add_u32_e32 v2, 0x840, v0
	ds_write2_b32 v2, v14, v15 offset1:1
	v_add_u32_e32 v2, 0x848, v0
	ds_write2_b32 v2, v16, v17 offset1:1
	v_add_u32_e32 v2, 0xc60, v0
	ds_write2_b32 v2, v10, v11 offset1:1
	v_add_u32_e32 v2, 0xc68, v0
	ds_write2_b32 v2, v12, v13 offset1:1
	v_add_u32_e32 v2, 0x1080, v0
	ds_write2_b32 v2, v22, v23 offset1:1
	v_add_u32_e32 v2, 0x1088, v0
	ds_write2_b32 v2, v24, v25 offset1:1
	v_add_u32_e32 v2, 0x14a0, v0
	ds_write2_b32 v2, v18, v19 offset1:1
	v_add_u32_e32 v2, 0x14a8, v0
	ds_write2_b32 v2, v20, v21 offset1:1
	v_add_u32_e32 v2, 0x18c0, v0
	ds_write2_b32 v2, v30, v31 offset1:1
	v_add_u32_e32 v2, 0x18c8, v0
	ds_write2_b32 v2, v32, v33 offset1:1
	v_add_u32_e32 v2, 0x1ce0, v0
	v_add_u32_e32 v0, 0x1ce8, v0
	ds_write2_b32 v2, v26, v27 offset1:1
	ds_write2_b32 v0, v28, v29 offset1:1
	s_waitcnt lgkmcnt(0)
	v_lshl_add_u64 v[2:3], s[24:25], 1, v[52:53]
	v_cmp_gt_i32_e32 vcc, s31, v35
	s_and_saveexec_b64 s[4:5], vcc
	s_cbranch_execz .LBB0_339
	ds_read2_b32 v[4:5], v75 offset0:198 offset1:231
	ds_read2_b32 v[8:9], v75 offset0:132 offset1:165
	s_waitcnt lgkmcnt(1)
	v_cvt_pk_bf16_f32 v7, v4, v5
	ds_read2_b32 v[4:5], v75 offset0:66 offset1:99
	s_waitcnt lgkmcnt(1)
	v_cvt_pk_bf16_f32 v6, v8, v9
	ds_read2_b32 v[8:9], v75 offset1:33
	s_waitcnt lgkmcnt(1)
	v_cvt_pk_bf16_f32 v5, v4, v5
	s_waitcnt lgkmcnt(0)
	v_cvt_pk_bf16_f32 v4, v8, v9
	v_or_b32_e32 v8, s22, v35
	v_ashrrev_i32_e32 v9, 31, v8
	v_lshlrev_b64 v[8:9], 12, v[8:9]
	v_lshl_add_u64 v[8:9], v[2:3], 0, v[8:9]
	global_store_dwordx4 v[8:9], v[4:7], off
	s_or_b64 exec, exec, s[4:5]
	v_cmp_gt_i32_e32 vcc, s31, v69
	s_and_saveexec_b64 s[4:5], vcc
	s_cbranch_execnz .LBB0_340

; #define LAS __attribute__((address_space(3)))
; __device__ __forceinline__ unsigned pk2(float lo, float hi) { return f2bf(lo) | (f2bf(hi) << 16); }
; template <int MAPK>
; __device__ __forceinline__ void transpose_item(const float* W, int ldw, int k0, int n0, int ncnt, bf16* WT, int ldd, int dcol0, int moff, LAS float* scr, int lane, const float* gk) {
;     ...
;     const int c = lane & 7;
; #pragma unroll
;     for (int j = 0; j < 4; ++j) { const int n = (lane >> 3) + 8 * j; const LAS float* s = scr + (8 * c) * 33 + n;
;         v4u o; o.x = pk2(s[0 * 33], s[1 * 33]); o.y = pk2(s[2 * 33], s[3 * 33]); o.z = pk2(s[4 * 33], s[5 * 33]); o.w = pk2(s[6 * 33], s[7 * 33]);
;         const int sn = n0 + n - moff;
;         int drow;
;         if (MAPK == MAP_LIN) drow = sn; else if (MAPK == MAP_GATE) drow = 32 * (sn >> 4) + (sn & 15); else drow = 32 * (sn >> 4) + 16 + (sn & 15);
;         if (n < ncnt) *(v4u*)(WT + (size_t)drow * ldd + dcol0 + k0 + 8 * c) = o; }
.LBB0_338:
	ds_read2_b32 v[4:5], v75 offset0:214 offset1:247
	ds_read2_b32 v[8:9], v75 offset0:148 offset1:181
	s_waitcnt lgkmcnt(1)
	v_cvt_pk_bf16_f32 v7, v4, v5
	ds_read2_b32 v[4:5], v75 offset0:82 offset1:115
	s_waitcnt lgkmcnt(1)
	v_cvt_pk_bf16_f32 v6, v8, v9
	ds_read2_b32 v[8:9], v75 offset0:16 offset1:49
	s_waitcnt lgkmcnt(1)
	v_cvt_pk_bf16_f32 v5, v4, v5
	s_waitcnt lgkmcnt(0)
	v_cvt_pk_bf16_f32 v4, v8, v9
	v_or_b32_e32 v8, s22, v71
	v_ashrrev_i32_e32 v9, 31, v8
	v_lshlrev_b64 v[8:9], 12, v[8:9]
	v_lshl_add_u64 v[8:9], v[2:3], 0, v[8:9]
	global_store_dwordx4 v[8:9], v[4:7], off
	s_or_b64 exec, exec, s[4:5]
	v_cmp_gt_i32_e32 vcc, s31, v73
	s_and_saveexec_b64 s[4:5], vcc
	s_cbranch_execnz .LBB0_342
	s_branch .LBB0_343

; #define LAS __attribute__((address_space(3)))
; __device__ __forceinline__ unsigned pk2(float lo, float hi) { return f2bf(lo) | (f2bf(hi) << 16); }
; template <int MAPK>
; __device__ __forceinline__ void transpose_item(const float* W, int ldw, int k0, int n0, int ncnt, bf16* WT, int ldd, int dcol0, int moff, LAS float* scr, int lane, const float* gk) {
;     ...
;     const int c = lane & 7;
; #pragma unroll
;     for (int j = 0; j < 4; ++j) { const int n = (lane >> 3) + 8 * j; const LAS float* s = scr + (8 * c) * 33 + n;
;         v4u o; o.x = pk2(s[0 * 33], s[1 * 33]); o.y = pk2(s[2 * 33], s[3 * 33]); o.z = pk2(s[4 * 33], s[5 * 33]); o.w = pk2(s[6 * 33], s[7 * 33]);
;         const int sn = n0 + n - moff;
;         int drow;
;         if (MAPK == MAP_LIN) drow = sn; else if (MAPK == MAP_GATE) drow = 32 * (sn >> 4) + (sn & 15); else drow = 32 * (sn >> 4) + 16 + (sn & 15);
;         if (n < ncnt) *(v4u*)(WT + (size_t)drow * ldd + dcol0 + k0 + 8 * c) = o; }
.LBB0_340:
	ds_read2_b32 v[4:5], v75 offset0:206 offset1:239
	ds_read2_b32 v[8:9], v75 offset0:140 offset1:173
	s_waitcnt lgkmcnt(1)
	v_cvt_pk_bf16_f32 v7, v4, v5
	ds_read2_b32 v[4:5], v75 offset0:74 offset1:107
	s_waitcnt lgkmcnt(1)
	v_cvt_pk_bf16_f32 v6, v8, v9
	ds_read2_b32 v[8:9], v75 offset0:8 offset1:41
	s_waitcnt lgkmcnt(1)
	v_cvt_pk_bf16_f32 v5, v4, v5
	s_waitcnt lgkmcnt(0)
	v_cvt_pk_bf16_f32 v4, v8, v9
	v_or_b32_e32 v8, s22, v69
	v_ashrrev_i32_e32 v9, 31, v8
	v_lshlrev_b64 v[8:9], 12, v[8:9]
	v_lshl_add_u64 v[8:9], v[2:3], 0, v[8:9]
	global_store_dwordx4 v[8:9], v[4:7], off
	s_or_b64 exec, exec, s[4:5]
	v_cmp_gt_i32_e32 vcc, s31, v71
	s_and_saveexec_b64 s[4:5], vcc
	s_cbranch_execnz .LBB0_338

; #define LAS __attribute__((address_space(3)))
; __device__ __forceinline__ unsigned pk2(float lo, float hi) { return f2bf(lo) | (f2bf(hi) << 16); }
; template <int MAPK>
; __device__ __forceinline__ void transpose_item(const float* W, int ldw, int k0, int n0, int ncnt, bf16* WT, int ldd, int dcol0, int moff, LAS float* scr, int lane, const float* gk) {
;     ...
;     const int c = lane & 7;
; #pragma unroll
;     for (int j = 0; j < 4; ++j) { const int n = (lane >> 3) + 8 * j; const LAS float* s = scr + (8 * c) * 33 + n;
;         v4u o; o.x = pk2(s[0 * 33], s[1 * 33]); o.y = pk2(s[2 * 33], s[3 * 33]); o.z = pk2(s[4 * 33], s[5 * 33]); o.w = pk2(s[6 * 33], s[7 * 33]);
;         const int sn = n0 + n - moff;
;         int drow;
;         if (MAPK == MAP_LIN) drow = sn; else if (MAPK == MAP_GATE) drow = 32 * (sn >> 4) + (sn & 15); else drow = 32 * (sn >> 4) + 16 + (sn & 15);
;         if (n < ncnt) *(v4u*)(WT + (size_t)drow * ldd + dcol0 + k0 + 8 * c) = o; }
.LBB0_342:
	ds_read2_b32 v[4:5], v75 offset0:222 offset1:255
	ds_read2_b32 v[8:9], v75 offset0:156 offset1:189
	s_waitcnt lgkmcnt(1)
	v_cvt_pk_bf16_f32 v7, v4, v5
	ds_read2_b32 v[4:5], v75 offset0:90 offset1:123
	s_waitcnt lgkmcnt(1)
	v_cvt_pk_bf16_f32 v6, v8, v9
	ds_read2_b32 v[8:9], v75 offset0:24 offset1:57
	s_waitcnt lgkmcnt(1)
	v_cvt_pk_bf16_f32 v5, v4, v5
	s_waitcnt lgkmcnt(0)
	v_cvt_pk_bf16_f32 v4, v8, v9
	v_or_b32_e32 v8, s22, v73
	v_ashrrev_i32_e32 v9, 31, v8
	v_lshlrev_b64 v[8:9], 12, v[8:9]
	v_lshl_add_u64 v[2:3], v[2:3], 0, v[8:9]
	global_store_dwordx4 v[2:3], v[4:7], off

; #define LAS __attribute__((address_space(3)))
; #define LDS_WAIT() asm volatile("s_waitcnt lgkmcnt(0)" ::: "memory")
; __device__ __forceinline__ unsigned pk2(float lo, float hi) { return f2bf(lo) | (f2bf(hi) << 16); }
; template <int MAPK>
; __device__ __forceinline__ void transpose_item(const float* W, int ldw, int k0, int n0, int ncnt, bf16* WT, int ldd, int dcol0, int moff, LAS float* scr, int lane, const float* gk) {
;     ...
;       for (int j = 0; j < 8; ++j) { LAS float* d = scr + (8 * j + kr) * 33 + c4; d[0] = v[j].x; d[1] = v[j].y; d[2] = v[j].z; d[3] = v[j].w; } }
;     LDS_WAIT(); asm volatile("" ::: "memory");
;     const int c = lane & 7;
; #pragma unroll
;     for (int j = 0; j < 4; ++j) { const int n = (lane >> 3) + 8 * j; const LAS float* s = scr + (8 * c) * 33 + n;
;         v4u o; o.x = pk2(s[0 * 33], s[1 * 33]); o.y = pk2(s[2 * 33], s[3 * 33]); o.z = pk2(s[4 * 33], s[5 * 33]); o.w = pk2(s[6 * 33], s[7 * 33]);
;         const int sn = n0 + n - moff;
;         int drow;
;         if (MAPK == MAP_LIN) drow = sn; else if (MAPK == MAP_GATE) drow = 32 * (sn >> 4) + (sn & 15); else drow = 32 * (sn >> 4) + 16 + (sn & 15);
;         if (n < ncnt) *(v4u*)(WT + (size_t)drow * ldd + dcol0 + k0 + 8 * c) = o; }
.LBB0_364:
	s_or_b64 exec, exec, s[26:27]
	s_waitcnt vmcnt(0)
	v_add_u32_e32 v0, v37, v67
	v_add_u32_e32 v64, 0x420, v0
	s_ashr_i32 s25, s24, 31
	ds_write2_b32 v0, v2, v3 offset1:1
	ds_write2_b32 v0, v4, v5 offset0:2 offset1:3
	ds_write2_b32 v64, v6, v7 offset1:1
	v_add_u32_e32 v2, 0x428, v0
	ds_write2_b32 v2, v8, v9 offset1:1
	v_add_u32_e32 v2, 0x840, v0
	ds_write2_b32 v2, v14, v15 offset1:1
	v_add_u32_e32 v2, 0x848, v0
	ds_write2_b32 v2, v16, v17 offset1:1
	v_add_u32_e32 v2, 0xc60, v0
	ds_write2_b32 v2, v10, v11 offset1:1
	v_add_u32_e32 v2, 0xc68, v0
	ds_write2_b32 v2, v12, v13 offset1:1
	v_add_u32_e32 v2, 0x1080, v0
	ds_write2_b32 v2, v22, v23 offset1:1
	v_add_u32_e32 v2, 0x1088, v0
	ds_write2_b32 v2, v24, v25 offset1:1
	v_add_u32_e32 v2, 0x14a0, v0
	ds_write2_b32 v2, v18, v19 offset1:1
	v_add_u32_e32 v2, 0x14a8, v0
	ds_write2_b32 v2, v20, v21 offset1:1
	v_add_u32_e32 v2, 0x18c0, v0
	ds_write2_b32 v2, v30, v31 offset1:1
	v_add_u32_e32 v2, 0x18c8, v0
	ds_write2_b32 v2, v32, v33 offset1:1
	v_add_u32_e32 v2, 0x1ce0, v0
	v_add_u32_e32 v0, 0x1ce8, v0
	ds_write2_b32 v2, v26, v27 offset1:1
	ds_write2_b32 v0, v28, v29 offset1:1
	s_waitcnt lgkmcnt(0)
	v_lshl_add_u64 v[2:3], s[24:25], 1, v[54:55]
	v_cmp_gt_i32_e32 vcc, s30, v35
	s_and_saveexec_b64 s[4:5], vcc
	s_cbranch_execz .LBB0_368
	ds_read2_b32 v[4:5], v75 offset0:198 offset1:231
	ds_read2_b32 v[8:9], v75 offset0:132 offset1:165
	s_waitcnt lgkmcnt(1)
	v_cvt_pk_bf16_f32 v7, v4, v5
	ds_read2_b32 v[4:5], v75 offset0:66 offset1:99
	s_waitcnt lgkmcnt(1)
	v_cvt_pk_bf16_f32 v6, v8, v9
	ds_read2_b32 v[8:9], v75 offset1:33
	s_waitcnt lgkmcnt(1)
	v_cvt_pk_bf16_f32 v5, v4, v5
	s_waitcnt lgkmcnt(0)
	v_cvt_pk_bf16_f32 v4, v8, v9
	v_or_b32_e32 v8, s22, v35
	v_ashrrev_i32_e32 v9, 31, v8
	v_lshlrev_b64 v[8:9], 12, v[8:9]
	v_lshl_add_u64 v[8:9], v[2:3], 0, v[8:9]
	global_store_dwordx4 v[8:9], v[4:7], off
	s_or_b64 exec, exec, s[4:5]
	v_cmp_gt_i32_e32 vcc, s30, v69
	s_and_saveexec_b64 s[4:5], vcc
	s_cbranch_execnz .LBB0_369

; #define LAS __attribute__((address_space(3)))
; __device__ __forceinline__ unsigned pk2(float lo, float hi) { return f2bf(lo) | (f2bf(hi) << 16); }
; template <int MAPK>
; __device__ __forceinline__ void transpose_item(const float* W, int ldw, int k0, int n0, int ncnt, bf16* WT, int ldd, int dcol0, int moff, LAS float* scr, int lane, const float* gk) {
;     ...
;     const int c = lane & 7;
; #pragma unroll
;     for (int j = 0; j < 4; ++j) { const int n = (lane >> 3) + 8 * j; const LAS float* s = scr + (8 * c) * 33 + n;
;         v4u o; o.x = pk2(s[0 * 33], s[1 * 33]); o.y = pk2(s[2 * 33], s[3 * 33]); o.z = pk2(s[4 * 33], s[5 * 33]); o.w = pk2(s[6 * 33], s[7 * 33]);
;         const int sn = n0 + n - moff;
;         int drow;
;         if (MAPK == MAP_LIN) drow = sn; else if (MAPK == MAP_GATE) drow = 32 * (sn >> 4) + (sn & 15); else drow = 32 * (sn >> 4) + 16 + (sn & 15);
;         if (n < ncnt) *(v4u*)(WT + (size_t)drow * ldd + dcol0 + k0 + 8 * c) = o; }
.LBB0_367:
	ds_read2_b32 v[4:5], v75 offset0:214 offset1:247
	ds_read2_b32 v[8:9], v75 offset0:148 offset1:181
	s_waitcnt lgkmcnt(1)
	v_cvt_pk_bf16_f32 v7, v4, v5
	ds_read2_b32 v[4:5], v75 offset0:82 offset1:115
	s_waitcnt lgkmcnt(1)
	v_cvt_pk_bf16_f32 v6, v8, v9
	ds_read2_b32 v[8:9], v75 offset0:16 offset1:49
	s_waitcnt lgkmcnt(1)
	v_cvt_pk_bf16_f32 v5, v4, v5
	s_waitcnt lgkmcnt(0)
	v_cvt_pk_bf16_f32 v4, v8, v9
	v_or_b32_e32 v8, s22, v71
	v_ashrrev_i32_e32 v9, 31, v8
	v_lshlrev_b64 v[8:9], 12, v[8:9]
	v_lshl_add_u64 v[8:9], v[2:3], 0, v[8:9]
	global_store_dwordx4 v[8:9], v[4:7], off
	s_or_b64 exec, exec, s[4:5]
	v_cmp_gt_i32_e32 vcc, s30, v73
	s_and_saveexec_b64 s[4:5], vcc
	s_cbranch_execnz .LBB0_371
	s_branch .LBB0_372

; #define LAS __attribute__((address_space(3)))
; __device__ __forceinline__ unsigned pk2(float lo, float hi) { return f2bf(lo) | (f2bf(hi) << 16); }
; template <int MAPK>
; __device__ __forceinline__ void transpose_item(const float* W, int ldw, int k0, int n0, int ncnt, bf16* WT, int ldd, int dcol0, int moff, LAS float* scr, int lane, const float* gk) {
;     ...
;     const int c = lane & 7;
; #pragma unroll
;     for (int j = 0; j < 4; ++j) { const int n = (lane >> 3) + 8 * j; const LAS float* s = scr + (8 * c) * 33 + n;
;         v4u o; o.x = pk2(s[0 * 33], s[1 * 33]); o.y = pk2(s[2 * 33], s[3 * 33]); o.z = pk2(s[4 * 33], s[5 * 33]); o.w = pk2(s[6 * 33], s[7 * 33]);
;         const int sn = n0 + n - moff;
;         int drow;
;         if (MAPK == MAP_LIN) drow = sn; else if (MAPK == MAP_GATE) drow = 32 * (sn >> 4) + (sn & 15); else drow = 32 * (sn >> 4) + 16 + (sn & 15);
;         if (n < ncnt) *(v4u*)(WT + (size_t)drow * ldd + dcol0 + k0 + 8 * c) = o; }
.LBB0_369:
	ds_read2_b32 v[4:5], v75 offset0:206 offset1:239
	ds_read2_b32 v[8:9], v75 offset0:140 offset1:173
	s_waitcnt lgkmcnt(1)
	v_cvt_pk_bf16_f32 v7, v4, v5
	ds_read2_b32 v[4:5], v75 offset0:74 offset1:107
	s_waitcnt lgkmcnt(1)
	v_cvt_pk_bf16_f32 v6, v8, v9
	ds_read2_b32 v[8:9], v75 offset0:8 offset1:41
	s_waitcnt lgkmcnt(1)
	v_cvt_pk_bf16_f32 v5, v4, v5
	s_waitcnt lgkmcnt(0)
	v_cvt_pk_bf16_f32 v4, v8, v9
	v_or_b32_e32 v8, s22, v69
	v_ashrrev_i32_e32 v9, 31, v8
	v_lshlrev_b64 v[8:9], 12, v[8:9]
	v_lshl_add_u64 v[8:9], v[2:3], 0, v[8:9]
	global_store_dwordx4 v[8:9], v[4:7], off
	s_or_b64 exec, exec, s[4:5]
	v_cmp_gt_i32_e32 vcc, s30, v71
	s_and_saveexec_b64 s[4:5], vcc
	s_cbranch_execnz .LBB0_367

; #define LAS __attribute__((address_space(3)))
; #define LDS_WAIT() asm volatile("s_waitcnt lgkmcnt(0)" ::: "memory")
; __device__ __forceinline__ unsigned pk2(float lo, float hi) { return f2bf(lo) | (f2bf(hi) << 16); }
; template <int MAPK>
; __device__ __forceinline__ void transpose_item(const float* W, int ldw, int k0, int n0, int ncnt, bf16* WT, int ldd, int dcol0, int moff, LAS float* scr, int lane, const float* gk) {
;     ...
;       for (int j = 0; j < 8; ++j) { LAS float* d = scr + (8 * j + kr) * 33 + c4; d[0] = v[j].x; d[1] = v[j].y; d[2] = v[j].z; d[3] = v[j].w; } }
;     LDS_WAIT(); asm volatile("" ::: "memory");
;     const int c = lane & 7;
; #pragma unroll
;     for (int j = 0; j < 4; ++j) { const int n = (lane >> 3) + 8 * j; const LAS float* s = scr + (8 * c) * 33 + n;
;         v4u o; o.x = pk2(s[0 * 33], s[1 * 33]); o.y = pk2(s[2 * 33], s[3 * 33]); o.z = pk2(s[4 * 33], s[5 * 33]); o.w = pk2(s[6 * 33], s[7 * 33]);
;         const int sn = n0 + n - moff;
;         int drow;
;         if (MAPK == MAP_LIN) drow = sn; else if (MAPK == MAP_GATE) drow = 32 * (sn >> 4) + (sn & 15); else drow = 32 * (sn >> 4) + 16 + (sn & 15);
;         if (n < ncnt) *(v4u*)(WT + (size_t)drow * ldd + dcol0 + k0 + 8 * c) = o; }
.LBB0_393:
	s_or_b64 exec, exec, s[26:27]
	s_waitcnt vmcnt(0)
	v_add_u32_e32 v0, v37, v67
	v_add_u32_e32 v64, 0x420, v0
	s_ashr_i32 s25, s24, 31
	ds_write2_b32 v0, v2, v3 offset1:1
	ds_write2_b32 v0, v4, v5 offset0:2 offset1:3
	ds_write2_b32 v64, v6, v7 offset1:1
	v_add_u32_e32 v2, 0x428, v0
	ds_write2_b32 v2, v8, v9 offset1:1
	v_add_u32_e32 v2, 0x840, v0
	ds_write2_b32 v2, v14, v15 offset1:1
	v_add_u32_e32 v2, 0x848, v0
	ds_write2_b32 v2, v16, v17 offset1:1
	v_add_u32_e32 v2, 0xc60, v0
	ds_write2_b32 v2, v10, v11 offset1:1
	v_add_u32_e32 v2, 0xc68, v0
	ds_write2_b32 v2, v12, v13 offset1:1
	v_add_u32_e32 v2, 0x1080, v0
	ds_write2_b32 v2, v22, v23 offset1:1
	v_add_u32_e32 v2, 0x1088, v0
	ds_write2_b32 v2, v24, v25 offset1:1
	v_add_u32_e32 v2, 0x14a0, v0
	ds_write2_b32 v2, v18, v19 offset1:1
	v_add_u32_e32 v2, 0x14a8, v0
	ds_write2_b32 v2, v20, v21 offset1:1
	v_add_u32_e32 v2, 0x18c0, v0
	ds_write2_b32 v2, v30, v31 offset1:1
	v_add_u32_e32 v2, 0x18c8, v0
	ds_write2_b32 v2, v32, v33 offset1:1
	v_add_u32_e32 v2, 0x1ce0, v0
	v_add_u32_e32 v0, 0x1ce8, v0
	ds_write2_b32 v2, v26, v27 offset1:1
	ds_write2_b32 v0, v28, v29 offset1:1
	s_waitcnt lgkmcnt(0)
	v_lshl_add_u64 v[2:3], s[24:25], 1, v[56:57]
	v_cmp_gt_i32_e32 vcc, s31, v35
	s_and_saveexec_b64 s[4:5], vcc
	s_cbranch_execz .LBB0_397
	ds_read2_b32 v[4:5], v75 offset0:198 offset1:231
	ds_read2_b32 v[8:9], v75 offset0:132 offset1:165
	s_waitcnt lgkmcnt(1)
	v_cvt_pk_bf16_f32 v7, v4, v5
	ds_read2_b32 v[4:5], v75 offset0:66 offset1:99
	s_waitcnt lgkmcnt(1)
	v_cvt_pk_bf16_f32 v6, v8, v9
	ds_read2_b32 v[8:9], v75 offset1:33
	s_waitcnt lgkmcnt(1)
	v_cvt_pk_bf16_f32 v5, v4, v5
	s_waitcnt lgkmcnt(0)
	v_cvt_pk_bf16_f32 v4, v8, v9
	v_or_b32_e32 v8, s22, v35
	v_ashrrev_i32_e32 v9, 31, v8
	v_lshlrev_b64 v[8:9], 12, v[8:9]
	v_lshl_add_u64 v[8:9], v[2:3], 0, v[8:9]
	global_store_dwordx4 v[8:9], v[4:7], off
	s_or_b64 exec, exec, s[4:5]
	v_cmp_gt_i32_e32 vcc, s31, v69
	s_and_saveexec_b64 s[4:5], vcc
	s_cbranch_execnz .LBB0_398

; #define LAS __attribute__((address_space(3)))
; #define LDS_WAIT() asm volatile("s_waitcnt lgkmcnt(0)" ::: "memory")
; __device__ __forceinline__ unsigned pk2(float lo, float hi) { return f2bf(lo) | (f2bf(hi) << 16); }
; template <int MAPK>
; __device__ __forceinline__ void transpose_item(const float* W, int ldw, int k0, int n0, int ncnt, bf16* WT, int ldd, int dcol0, int moff, LAS float* scr, int lane, const float* gk) {
;     ...
;           for (int j = 0; j < 8; ++j) gj[j] = gk[k0 + 8 * j + kr]; }
; #pragma unroll
;       for (int j = 0; j < 8; ++j) v[j] = (c4 < ncnt) ? *(const f32x4*)(wp + (size_t)(8 * j) * ldw) : (f32x4){0.f, 0.f, 0.f, 0.f};
;       asm volatile("" : "+v"(v[0]), "+v"(v[1]), "+v"(v[2]), "+v"(v[3]), "+v"(v[4]), "+v"(v[5]), "+v"(v[6]), "+v"(v[7]) :: "memory");
; #pragma unroll
;       for (int j = 0; j < 8; ++j) v[j] = v[j] * gj[j];
; #pragma unroll
;       for (int j = 0; j < 8; ++j) { LAS float* d = scr + (8 * j + kr) * 33 + c4; d[0] = v[j].x; d[1] = v[j].y; d[2] = v[j].z; d[3] = v[j].w; } }
;     LDS_WAIT(); asm volatile("" ::: "memory");
;     const int c = lane & 7;
; #pragma unroll
;     for (int j = 0; j < 4; ++j) { const int n = (lane >> 3) + 8 * j; const LAS float* s = scr + (8 * c) * 33 + n;
;         v4u o; o.x = pk2(s[0 * 33], s[1 * 33]); o.y = pk2(s[2 * 33], s[3 * 33]); o.z = pk2(s[4 * 33], s[5 * 33]); o.w = pk2(s[6 * 33], s[7 * 33]);
;         const int sn = n0 + n - moff;
;         int drow;
;         if (MAPK == MAP_LIN) drow = sn; else if (MAPK == MAP_GATE) drow = 32 * (sn >> 4) + (sn & 15); else drow = 32 * (sn >> 4) + 16 + (sn & 15);
;         if (n < ncnt) *(v4u*)(WT + (size_t)drow * ldd + dcol0 + k0 + 8 * c) = o; }
.LBB0_424:
	s_or_b64 exec, exec, s[24:25]
	s_waitcnt vmcnt(0)
	v_lshlrev_b32_e32 v91, 2, v35
	ds_bpermute_b32 v78, v91, v90
	ds_bpermute_b32 v76, v91, v90 offset:32
	ds_bpermute_b32 v74, v91, v90 offset:64
	ds_bpermute_b32 v72, v91, v90 offset:96
	ds_bpermute_b32 v70, v91, v90 offset:128
	ds_bpermute_b32 v68, v91, v90 offset:160
	ds_bpermute_b32 v66, v91, v90 offset:192
	ds_bpermute_b32 v64, v91, v90 offset:224
	s_waitcnt lgkmcnt(0)
	v_add_u32_e32 v0, v37, v67
	v_pk_mul_f32 v[2:3], v[78:79], v[2:3] op_sel_hi:[0,1]
	v_pk_mul_f32 v[4:5], v[78:79], v[4:5] op_sel_hi:[0,1]
	v_pk_mul_f32 v[6:7], v[76:77], v[6:7] op_sel_hi:[0,1]
	ds_write2_b32 v0, v2, v3 offset1:1
	ds_write2_b32 v0, v4, v5 offset0:2 offset1:3
	v_add_u32_e32 v2, 0x420, v0
	v_pk_mul_f32 v[8:9], v[76:77], v[8:9] op_sel_hi:[0,1]
	ds_write2_b32 v2, v6, v7 offset1:1
	v_add_u32_e32 v2, 0x428, v0
	v_pk_mul_f32 v[14:15], v[74:75], v[14:15] op_sel_hi:[0,1]
	ds_write2_b32 v2, v8, v9 offset1:1
	v_add_u32_e32 v2, 0x840, v0
	v_pk_mul_f32 v[16:17], v[74:75], v[16:17] op_sel_hi:[0,1]
	ds_write2_b32 v2, v14, v15 offset1:1
	v_add_u32_e32 v2, 0x848, v0
	v_pk_mul_f32 v[10:11], v[72:73], v[10:11] op_sel_hi:[0,1]
	ds_write2_b32 v2, v16, v17 offset1:1
	v_add_u32_e32 v2, 0xc60, v0
	v_pk_mul_f32 v[12:13], v[72:73], v[12:13] op_sel_hi:[0,1]
	ds_write2_b32 v2, v10, v11 offset1:1
	v_add_u32_e32 v2, 0xc68, v0
	v_pk_mul_f32 v[22:23], v[70:71], v[22:23] op_sel_hi:[0,1]
	ds_write2_b32 v2, v12, v13 offset1:1
	v_add_u32_e32 v2, 0x1080, v0
	v_pk_mul_f32 v[24:25], v[70:71], v[24:25] op_sel_hi:[0,1]
	ds_write2_b32 v2, v22, v23 offset1:1
	v_add_u32_e32 v2, 0x1088, v0
	v_pk_mul_f32 v[18:19], v[68:69], v[18:19] op_sel_hi:[0,1]
	ds_write2_b32 v2, v24, v25 offset1:1
	v_add_u32_e32 v2, 0x14a0, v0
	v_pk_mul_f32 v[20:21], v[68:69], v[20:21] op_sel_hi:[0,1]
	ds_write2_b32 v2, v18, v19 offset1:1
	v_add_u32_e32 v2, 0x14a8, v0
	v_pk_mul_f32 v[30:31], v[66:67], v[30:31] op_sel_hi:[0,1]
	ds_write2_b32 v2, v20, v21 offset1:1
	v_add_u32_e32 v2, 0x18c0, v0
	v_pk_mul_f32 v[32:33], v[66:67], v[32:33] op_sel_hi:[0,1]
	ds_write2_b32 v2, v30, v31 offset1:1
	v_add_u32_e32 v2, 0x18c8, v0
	v_pk_mul_f32 v[28:29], v[64:65], v[28:29] op_sel_hi:[0,1]
	v_pk_mul_f32 v[26:27], v[64:65], v[26:27] op_sel_hi:[0,1]
	ds_write2_b32 v2, v32, v33 offset1:1
	v_add_u32_e32 v2, 0x1ce0, v0
	v_add_u32_e32 v0, 0x1ce8, v0
	ds_write2_b32 v2, v26, v27 offset1:1
	ds_write2_b32 v0, v28, v29 offset1:1
	s_waitcnt lgkmcnt(0)
	s_ashr_i32 s23, s22, 31
	v_lshl_add_u64 v[2:3], s[22:23], 1, v[58:59]
	v_cmp_gt_i32_e32 vcc, s30, v35
	s_and_saveexec_b64 s[4:5], vcc
	s_cbranch_execz .LBB0_428
	ds_read2_b32 v[4:5], v75 offset0:198 offset1:231
	ds_read2_b32 v[8:9], v75 offset0:132 offset1:165
	s_movk_i32 s22, 0x1080
	s_waitcnt lgkmcnt(1)
	v_cvt_pk_bf16_f32 v7, v4, v5
	ds_read2_b32 v[4:5], v75 offset0:66 offset1:99
	s_waitcnt lgkmcnt(1)
	v_cvt_pk_bf16_f32 v6, v8, v9
	ds_read2_b32 v[8:9], v75 offset1:33
	s_waitcnt lgkmcnt(1)
	v_cvt_pk_bf16_f32 v5, v4, v5
	s_waitcnt lgkmcnt(0)
	v_cvt_pk_bf16_f32 v4, v8, v9
	v_lshl_or_b32 v0, s27, 6, v35
	v_mad_i64_i32 v[8:9], s[22:23], v0, s22, v[2:3]
	global_store_dwordx4 v[8:9], v[4:7], off
	s_or_b64 exec, exec, s[4:5]
	v_cmp_gt_i32_e32 vcc, s30, v69
	s_and_saveexec_b64 s[4:5], vcc
	s_cbranch_execnz .LBB0_429

; #define LAS __attribute__((address_space(3)))
; __device__ __forceinline__ unsigned pk2(float lo, float hi) { return f2bf(lo) | (f2bf(hi) << 16); }
; template <int MAPK>
; __device__ __forceinline__ void transpose_item(const float* W, int ldw, int k0, int n0, int ncnt, bf16* WT, int ldd, int dcol0, int moff, LAS float* scr, int lane, const float* gk) {
;     ...
;     const int c = lane & 7;
; #pragma unroll
;     for (int j = 0; j < 4; ++j) { const int n = (lane >> 3) + 8 * j; const LAS float* s = scr + (8 * c) * 33 + n;
;         v4u o; o.x = pk2(s[0 * 33], s[1 * 33]); o.y = pk2(s[2 * 33], s[3 * 33]); o.z = pk2(s[4 * 33], s[5 * 33]); o.w = pk2(s[6 * 33], s[7 * 33]);
;         const int sn = n0 + n - moff;
;         int drow;
;         if (MAPK == MAP_LIN) drow = sn; else if (MAPK == MAP_GATE) drow = 32 * (sn >> 4) + (sn & 15); else drow = 32 * (sn >> 4) + 16 + (sn & 15);
;         if (n < ncnt) *(v4u*)(WT + (size_t)drow * ldd + dcol0 + k0 + 8 * c) = o; }
.LBB0_427:
	ds_read2_b32 v[4:5], v75 offset0:214 offset1:247
	ds_read2_b32 v[8:9], v75 offset0:148 offset1:181
	s_movk_i32 s22, 0x1080
	s_waitcnt lgkmcnt(1)
	v_cvt_pk_bf16_f32 v7, v4, v5
	ds_read2_b32 v[4:5], v75 offset0:82 offset1:115
	s_waitcnt lgkmcnt(1)
	v_cvt_pk_bf16_f32 v6, v8, v9
	ds_read2_b32 v[8:9], v75 offset0:16 offset1:49
	s_waitcnt lgkmcnt(1)
	v_cvt_pk_bf16_f32 v5, v4, v5
	s_waitcnt lgkmcnt(0)
	v_cvt_pk_bf16_f32 v4, v8, v9
	v_lshl_or_b32 v0, s27, 6, v77
	v_mad_i64_i32 v[8:9], s[22:23], v0, s22, v[2:3]
	global_store_dwordx4 v[8:9], v[4:7], off
	s_or_b64 exec, exec, s[4:5]
	v_cmp_gt_i32_e32 vcc, s30, v73
	s_and_saveexec_b64 s[4:5], vcc
	s_cbranch_execnz .LBB0_431
	s_branch .LBB0_432

; #define LAS __attribute__((address_space(3)))
; __device__ __forceinline__ unsigned pk2(float lo, float hi) { return f2bf(lo) | (f2bf(hi) << 16); }
; template <int MAPK>
; __device__ __forceinline__ void transpose_item(const float* W, int ldw, int k0, int n0, int ncnt, bf16* WT, int ldd, int dcol0, int moff, LAS float* scr, int lane, const float* gk) {
;     ...
;     const int c = lane & 7;
; #pragma unroll
;     for (int j = 0; j < 4; ++j) { const int n = (lane >> 3) + 8 * j; const LAS float* s = scr + (8 * c) * 33 + n;
;         v4u o; o.x = pk2(s[0 * 33], s[1 * 33]); o.y = pk2(s[2 * 33], s[3 * 33]); o.z = pk2(s[4 * 33], s[5 * 33]); o.w = pk2(s[6 * 33], s[7 * 33]);
;         const int sn = n0 + n - moff;
;         int drow;
;         if (MAPK == MAP_LIN) drow = sn; else if (MAPK == MAP_GATE) drow = 32 * (sn >> 4) + (sn & 15); else drow = 32 * (sn >> 4) + 16 + (sn & 15);
;         if (n < ncnt) *(v4u*)(WT + (size_t)drow * ldd + dcol0 + k0 + 8 * c) = o; }
.LBB0_429:
	ds_read2_b32 v[4:5], v75 offset0:206 offset1:239
	ds_read2_b32 v[8:9], v75 offset0:140 offset1:173
	s_movk_i32 s22, 0x1080
	s_waitcnt lgkmcnt(1)
	v_cvt_pk_bf16_f32 v7, v4, v5
	ds_read2_b32 v[4:5], v75 offset0:74 offset1:107
	s_waitcnt lgkmcnt(1)
	v_cvt_pk_bf16_f32 v6, v8, v9
	ds_read2_b32 v[8:9], v75 offset0:8 offset1:41
	s_waitcnt lgkmcnt(1)
	v_cvt_pk_bf16_f32 v5, v4, v5
	s_waitcnt lgkmcnt(0)
	v_cvt_pk_bf16_f32 v4, v8, v9
	v_lshl_or_b32 v0, s27, 6, v69
	v_mad_i64_i32 v[8:9], s[22:23], v0, s22, v[2:3]
	global_store_dwordx4 v[8:9], v[4:7], off
	s_or_b64 exec, exec, s[4:5]
	v_cmp_gt_i32_e32 vcc, s30, v71
	s_and_saveexec_b64 s[4:5], vcc
	s_cbranch_execnz .LBB0_427

; #define LAS __attribute__((address_space(3)))
; __device__ __forceinline__ unsigned pk2(float lo, float hi) { return f2bf(lo) | (f2bf(hi) << 16); }
; template <int MAPK>
; __device__ __forceinline__ void transpose_item(const float* W, int ldw, int k0, int n0, int ncnt, bf16* WT, int ldd, int dcol0, int moff, LAS float* scr, int lane, const float* gk) {
;     ...
;     const int c = lane & 7;
; #pragma unroll
;     for (int j = 0; j < 4; ++j) { const int n = (lane >> 3) + 8 * j; const LAS float* s = scr + (8 * c) * 33 + n;
;         v4u o; o.x = pk2(s[0 * 33], s[1 * 33]); o.y = pk2(s[2 * 33], s[3 * 33]); o.z = pk2(s[4 * 33], s[5 * 33]); o.w = pk2(s[6 * 33], s[7 * 33]);
;         const int sn = n0 + n - moff;
;         int drow;
;         if (MAPK == MAP_LIN) drow = sn; else if (MAPK == MAP_GATE) drow = 32 * (sn >> 4) + (sn & 15); else drow = 32 * (sn >> 4) + 16 + (sn & 15);
;         if (n < ncnt) *(v4u*)(WT + (size_t)drow * ldd + dcol0 + k0 + 8 * c) = o; }
.LBB0_431:
	ds_read2_b32 v[4:5], v75 offset0:222 offset1:255
	ds_read2_b32 v[8:9], v75 offset0:156 offset1:189
	s_movk_i32 s22, 0x1080
	s_waitcnt lgkmcnt(1)
	v_cvt_pk_bf16_f32 v7, v4, v5
	ds_read2_b32 v[4:5], v75 offset0:90 offset1:123
	s_waitcnt lgkmcnt(1)
	v_cvt_pk_bf16_f32 v6, v8, v9
	ds_read2_b32 v[8:9], v75 offset0:24 offset1:57
	s_waitcnt lgkmcnt(1)
	v_cvt_pk_bf16_f32 v5, v4, v5
	s_waitcnt lgkmcnt(0)
	v_cvt_pk_bf16_f32 v4, v8, v9
	v_lshl_or_b32 v0, s27, 6, v79
	v_mad_i64_i32 v[2:3], s[22:23], v0, s22, v[2:3]
	global_store_dwordx4 v[2:3], v[4:7], off

; #define LAS __attribute__((address_space(3)))
; #define LDS_WAIT() asm volatile("s_waitcnt lgkmcnt(0)" ::: "memory")
; __device__ __forceinline__ unsigned pk2(float lo, float hi) { return f2bf(lo) | (f2bf(hi) << 16); }
; template <int MAPK>
; __device__ __forceinline__ void transpose_item(const float* W, int ldw, int k0, int n0, int ncnt, bf16* WT, int ldd, int dcol0, int moff, LAS float* scr, int lane, const float* gk) {
;     ...
;           for (int j = 0; j < 8; ++j) gj[j] = gk[k0 + 8 * j + kr]; }
; #pragma unroll
;       for (int j = 0; j < 8; ++j) v[j] = (c4 < ncnt) ? *(const f32x4*)(wp + (size_t)(8 * j) * ldw) : (f32x4){0.f, 0.f, 0.f, 0.f};
;       asm volatile("" : "+v"(v[0]), "+v"(v[1]), "+v"(v[2]), "+v"(v[3]), "+v"(v[4]), "+v"(v[5]), "+v"(v[6]), "+v"(v[7]) :: "memory");
; #pragma unroll
;       for (int j = 0; j < 8; ++j) v[j] = v[j] * gj[j];
; #pragma unroll
;       for (int j = 0; j < 8; ++j) { LAS float* d = scr + (8 * j + kr) * 33 + c4; d[0] = v[j].x; d[1] = v[j].y; d[2] = v[j].z; d[3] = v[j].w; } }
;     LDS_WAIT(); asm volatile("" ::: "memory");
;     const int c = lane & 7;
; #pragma unroll
;     for (int j = 0; j < 4; ++j) { const int n = (lane >> 3) + 8 * j; const LAS float* s = scr + (8 * c) * 33 + n;
;         v4u o; o.x = pk2(s[0 * 33], s[1 * 33]); o.y = pk2(s[2 * 33], s[3 * 33]); o.z = pk2(s[4 * 33], s[5 * 33]); o.w = pk2(s[6 * 33], s[7 * 33]);
;         const int sn = n0 + n - moff;
;         int drow;
;         if (MAPK == MAP_LIN) drow = sn; else if (MAPK == MAP_GATE) drow = 32 * (sn >> 4) + (sn & 15); else drow = 32 * (sn >> 4) + 16 + (sn & 15);
;         if (n < ncnt) *(v4u*)(WT + (size_t)drow * ldd + dcol0 + k0 + 8 * c) = o; }
.LBB0_455:
	s_or_b64 exec, exec, s[24:25]
	s_waitcnt vmcnt(0)
	v_lshlrev_b32_e32 v91, 2, v35
	ds_bpermute_b32 v78, v91, v90
	ds_bpermute_b32 v76, v91, v90 offset:32
	ds_bpermute_b32 v74, v91, v90 offset:64
	ds_bpermute_b32 v72, v91, v90 offset:96
	ds_bpermute_b32 v70, v91, v90 offset:128
	ds_bpermute_b32 v68, v91, v90 offset:160
	ds_bpermute_b32 v66, v91, v90 offset:192
	ds_bpermute_b32 v64, v91, v90 offset:224
	s_waitcnt lgkmcnt(0)
	v_add_u32_e32 v0, v37, v67
	v_pk_mul_f32 v[2:3], v[78:79], v[2:3] op_sel_hi:[0,1]
	v_pk_mul_f32 v[4:5], v[78:79], v[4:5] op_sel_hi:[0,1]
	v_pk_mul_f32 v[6:7], v[76:77], v[6:7] op_sel_hi:[0,1]
	ds_write2_b32 v0, v2, v3 offset1:1
	ds_write2_b32 v0, v4, v5 offset0:2 offset1:3
	v_add_u32_e32 v2, 0x420, v0
	v_pk_mul_f32 v[8:9], v[76:77], v[8:9] op_sel_hi:[0,1]
	ds_write2_b32 v2, v6, v7 offset1:1
	v_add_u32_e32 v2, 0x428, v0
	v_pk_mul_f32 v[14:15], v[74:75], v[14:15] op_sel_hi:[0,1]
	ds_write2_b32 v2, v8, v9 offset1:1
	v_add_u32_e32 v2, 0x840, v0
	v_pk_mul_f32 v[16:17], v[74:75], v[16:17] op_sel_hi:[0,1]
	ds_write2_b32 v2, v14, v15 offset1:1
	v_add_u32_e32 v2, 0x848, v0
	v_pk_mul_f32 v[10:11], v[72:73], v[10:11] op_sel_hi:[0,1]
	ds_write2_b32 v2, v16, v17 offset1:1
	v_add_u32_e32 v2, 0xc60, v0
	v_pk_mul_f32 v[12:13], v[72:73], v[12:13] op_sel_hi:[0,1]
	ds_write2_b32 v2, v10, v11 offset1:1
	v_add_u32_e32 v2, 0xc68, v0
	v_pk_mul_f32 v[22:23], v[70:71], v[22:23] op_sel_hi:[0,1]
	ds_write2_b32 v2, v12, v13 offset1:1
	v_add_u32_e32 v2, 0x1080, v0
	v_pk_mul_f32 v[24:25], v[70:71], v[24:25] op_sel_hi:[0,1]
	ds_write2_b32 v2, v22, v23 offset1:1
	v_add_u32_e32 v2, 0x1088, v0
	v_pk_mul_f32 v[18:19], v[68:69], v[18:19] op_sel_hi:[0,1]
	ds_write2_b32 v2, v24, v25 offset1:1
	v_add_u32_e32 v2, 0x14a0, v0
	v_pk_mul_f32 v[20:21], v[68:69], v[20:21] op_sel_hi:[0,1]
	ds_write2_b32 v2, v18, v19 offset1:1
	v_add_u32_e32 v2, 0x14a8, v0
	v_pk_mul_f32 v[30:31], v[66:67], v[30:31] op_sel_hi:[0,1]
	ds_write2_b32 v2, v20, v21 offset1:1
	v_add_u32_e32 v2, 0x18c0, v0
	v_pk_mul_f32 v[32:33], v[66:67], v[32:33] op_sel_hi:[0,1]
	ds_write2_b32 v2, v30, v31 offset1:1
	v_add_u32_e32 v2, 0x18c8, v0
	v_pk_mul_f32 v[28:29], v[64:65], v[28:29] op_sel_hi:[0,1]
	v_pk_mul_f32 v[26:27], v[64:65], v[26:27] op_sel_hi:[0,1]
	ds_write2_b32 v2, v32, v33 offset1:1
	v_add_u32_e32 v2, 0x1ce0, v0
	v_add_u32_e32 v0, 0x1ce8, v0
	ds_write2_b32 v2, v26, v27 offset1:1
	ds_write2_b32 v0, v28, v29 offset1:1
	s_waitcnt lgkmcnt(0)
	s_ashr_i32 s23, s22, 31
	v_lshl_add_u64 v[2:3], s[22:23], 1, v[58:59]
	v_cmp_gt_i32_e32 vcc, s30, v35
	s_and_saveexec_b64 s[4:5], vcc
	s_cbranch_execz .LBB0_459
	ds_read2_b32 v[4:5], v75 offset0:198 offset1:231
	ds_read2_b32 v[8:9], v75 offset0:132 offset1:165
	s_movk_i32 s22, 0x1080
	s_waitcnt lgkmcnt(1)
	v_cvt_pk_bf16_f32 v7, v4, v5
	ds_read2_b32 v[4:5], v75 offset0:66 offset1:99
	s_waitcnt lgkmcnt(1)
	v_cvt_pk_bf16_f32 v6, v8, v9
	ds_read2_b32 v[8:9], v75 offset1:33
	s_waitcnt lgkmcnt(1)
	v_cvt_pk_bf16_f32 v5, v4, v5
	s_waitcnt lgkmcnt(0)
	v_cvt_pk_bf16_f32 v4, v8, v9
	v_lshl_or_b32 v0, s26, 6, v71
	v_mad_i64_i32 v[8:9], s[22:23], v0, s22, v[2:3]
	global_store_dwordx4 v[8:9], v[4:7], off
	s_or_b64 exec, exec, s[4:5]
	v_cmp_gt_i32_e32 vcc, s30, v69
	s_and_saveexec_b64 s[4:5], vcc
	s_cbranch_execnz .LBB0_460

; #define LAS __attribute__((address_space(3)))
; __device__ __forceinline__ unsigned pk2(float lo, float hi) { return f2bf(lo) | (f2bf(hi) << 16); }
; template <int MAPK>
; __device__ __forceinline__ void transpose_item(const float* W, int ldw, int k0, int n0, int ncnt, bf16* WT, int ldd, int dcol0, int moff, LAS float* scr, int lane, const float* gk) {
;     ...
;     const int c = lane & 7;
; #pragma unroll
;     for (int j = 0; j < 4; ++j) { const int n = (lane >> 3) + 8 * j; const LAS float* s = scr + (8 * c) * 33 + n;
;         v4u o; o.x = pk2(s[0 * 33], s[1 * 33]); o.y = pk2(s[2 * 33], s[3 * 33]); o.z = pk2(s[4 * 33], s[5 * 33]); o.w = pk2(s[6 * 33], s[7 * 33]);
;         const int sn = n0 + n - moff;
;         int drow;
;         if (MAPK == MAP_LIN) drow = sn; else if (MAPK == MAP_GATE) drow = 32 * (sn >> 4) + (sn & 15); else drow = 32 * (sn >> 4) + 16 + (sn & 15);
;         if (n < ncnt) *(v4u*)(WT + (size_t)drow * ldd + dcol0 + k0 + 8 * c) = o; }
.LBB0_458:
	ds_read2_b32 v[4:5], v75 offset0:214 offset1:247
	ds_read2_b32 v[8:9], v75 offset0:148 offset1:181
	s_movk_i32 s22, 0x1080
	s_waitcnt lgkmcnt(1)
	v_cvt_pk_bf16_f32 v7, v4, v5
	ds_read2_b32 v[4:5], v75 offset0:82 offset1:115
	s_waitcnt lgkmcnt(1)
	v_cvt_pk_bf16_f32 v6, v8, v9
	ds_read2_b32 v[8:9], v75 offset0:16 offset1:49
	s_waitcnt lgkmcnt(1)
	v_cvt_pk_bf16_f32 v5, v4, v5
	s_waitcnt lgkmcnt(0)
	v_cvt_pk_bf16_f32 v4, v8, v9
	v_lshl_or_b32 v0, s26, 6, v82
	v_mad_i64_i32 v[8:9], s[22:23], v0, s22, v[2:3]
	global_store_dwordx4 v[8:9], v[4:7], off
	s_or_b64 exec, exec, s[4:5]
	v_cmp_gt_i32_e32 vcc, s30, v73
	s_and_saveexec_b64 s[4:5], vcc
	s_cbranch_execnz .LBB0_462
	s_branch .LBB0_463

; #define LAS __attribute__((address_space(3)))
; __device__ __forceinline__ unsigned pk2(float lo, float hi) { return f2bf(lo) | (f2bf(hi) << 16); }
; template <int MAPK>
; __device__ __forceinline__ void transpose_item(const float* W, int ldw, int k0, int n0, int ncnt, bf16* WT, int ldd, int dcol0, int moff, LAS float* scr, int lane, const float* gk) {
;     ...
;     const int c = lane & 7;
; #pragma unroll
;     for (int j = 0; j < 4; ++j) { const int n = (lane >> 3) + 8 * j; const LAS float* s = scr + (8 * c) * 33 + n;
;         v4u o; o.x = pk2(s[0 * 33], s[1 * 33]); o.y = pk2(s[2 * 33], s[3 * 33]); o.z = pk2(s[4 * 33], s[5 * 33]); o.w = pk2(s[6 * 33], s[7 * 33]);
;         const int sn = n0 + n - moff;
;         int drow;
;         if (MAPK == MAP_LIN) drow = sn; else if (MAPK == MAP_GATE) drow = 32 * (sn >> 4) + (sn & 15); else drow = 32 * (sn >> 4) + 16 + (sn & 15);
;         if (n < ncnt) *(v4u*)(WT + (size_t)drow * ldd + dcol0 + k0 + 8 * c) = o; }
.LBB0_460:
	ds_read2_b32 v[4:5], v75 offset0:206 offset1:239
	ds_read2_b32 v[8:9], v75 offset0:140 offset1:173
	s_movk_i32 s22, 0x1080
	s_waitcnt lgkmcnt(1)
	v_cvt_pk_bf16_f32 v7, v4, v5
	ds_read2_b32 v[4:5], v75 offset0:74 offset1:107
	s_waitcnt lgkmcnt(1)
	v_cvt_pk_bf16_f32 v6, v8, v9
	ds_read2_b32 v[8:9], v75 offset0:8 offset1:41
	s_waitcnt lgkmcnt(1)
	v_cvt_pk_bf16_f32 v5, v4, v5
	s_waitcnt lgkmcnt(0)
	v_cvt_pk_bf16_f32 v4, v8, v9
	v_lshl_or_b32 v0, s26, 6, v73
	v_mad_i64_i32 v[8:9], s[22:23], v0, s22, v[2:3]
	global_store_dwordx4 v[8:9], v[4:7], off
	s_or_b64 exec, exec, s[4:5]
	v_cmp_gt_i32_e32 vcc, s30, v71
	s_and_saveexec_b64 s[4:5], vcc
	s_cbranch_execnz .LBB0_458

; #define LAS __attribute__((address_space(3)))
; __device__ __forceinline__ unsigned pk2(float lo, float hi) { return f2bf(lo) | (f2bf(hi) << 16); }
; template <int MAPK>
; __device__ __forceinline__ void transpose_item(const float* W, int ldw, int k0, int n0, int ncnt, bf16* WT, int ldd, int dcol0, int moff, LAS float* scr, int lane, const float* gk) {
;     ...
;     const int c = lane & 7;
; #pragma unroll
;     for (int j = 0; j < 4; ++j) { const int n = (lane >> 3) + 8 * j; const LAS float* s = scr + (8 * c) * 33 + n;
;         v4u o; o.x = pk2(s[0 * 33], s[1 * 33]); o.y = pk2(s[2 * 33], s[3 * 33]); o.z = pk2(s[4 * 33], s[5 * 33]); o.w = pk2(s[6 * 33], s[7 * 33]);
;         const int sn = n0 + n - moff;
;         int drow;
;         if (MAPK == MAP_LIN) drow = sn; else if (MAPK == MAP_GATE) drow = 32 * (sn >> 4) + (sn & 15); else drow = 32 * (sn >> 4) + 16 + (sn & 15);
;         if (n < ncnt) *(v4u*)(WT + (size_t)drow * ldd + dcol0 + k0 + 8 * c) = o; }
.LBB0_462:
	ds_read2_b32 v[4:5], v75 offset0:222 offset1:255
	ds_read2_b32 v[8:9], v75 offset0:156 offset1:189
	s_movk_i32 s22, 0x1080
	s_waitcnt lgkmcnt(1)
	v_cvt_pk_bf16_f32 v7, v4, v5
	ds_read2_b32 v[4:5], v75 offset0:90 offset1:123
	s_waitcnt lgkmcnt(1)
	v_cvt_pk_bf16_f32 v6, v8, v9
	ds_read2_b32 v[8:9], v75 offset0:24 offset1:57
	s_waitcnt lgkmcnt(1)
	v_cvt_pk_bf16_f32 v5, v4, v5
	s_waitcnt lgkmcnt(0)
	v_cvt_pk_bf16_f32 v4, v8, v9
	v_lshl_or_b32 v0, s26, 6, v83
	v_mad_i64_i32 v[2:3], s[22:23], v0, s22, v[2:3]
	global_store_dwordx4 v[2:3], v[4:7], off

; #define LAS __attribute__((address_space(3)))
; #define LDS_WAIT() asm volatile("s_waitcnt lgkmcnt(0)" ::: "memory")
; __device__ __forceinline__ unsigned pk2(float lo, float hi) { return f2bf(lo) | (f2bf(hi) << 16); }
; template <int MAPK>
; __device__ __forceinline__ void transpose_item(const float* W, int ldw, int k0, int n0, int ncnt, bf16* WT, int ldd, int dcol0, int moff, LAS float* scr, int lane, const float* gk) {
;     ...
;       for (int j = 0; j < 8; ++j) { LAS float* d = scr + (8 * j + kr) * 33 + c4; d[0] = v[j].x; d[1] = v[j].y; d[2] = v[j].z; d[3] = v[j].w; } }
;     LDS_WAIT(); asm volatile("" ::: "memory");
;     const int c = lane & 7;
; #pragma unroll
;     for (int j = 0; j < 4; ++j) { const int n = (lane >> 3) + 8 * j; const LAS float* s = scr + (8 * c) * 33 + n;
;         v4u o; o.x = pk2(s[0 * 33], s[1 * 33]); o.y = pk2(s[2 * 33], s[3 * 33]); o.z = pk2(s[4 * 33], s[5 * 33]); o.w = pk2(s[6 * 33], s[7 * 33]);
;         const int sn = n0 + n - moff;
;         int drow;
;         if (MAPK == MAP_LIN) drow = sn; else if (MAPK == MAP_GATE) drow = 32 * (sn >> 4) + (sn & 15); else drow = 32 * (sn >> 4) + 16 + (sn & 15);
;         if (n < ncnt) *(v4u*)(WT + (size_t)drow * ldd + dcol0 + k0 + 8 * c) = o; }
.LBB0_480:
	s_or_b64 exec, exec, s[24:25]
	s_waitcnt vmcnt(0)
	v_add_u32_e32 v0, v37, v67
	v_add_u32_e32 v64, 0x420, v0
	s_ashr_i32 s23, s22, 31
	ds_write2_b32 v0, v2, v3 offset1:1
	ds_write2_b32 v0, v4, v5 offset0:2 offset1:3
	ds_write2_b32 v64, v6, v7 offset1:1
	v_add_u32_e32 v2, 0x428, v0
	ds_write2_b32 v2, v8, v9 offset1:1
	v_add_u32_e32 v2, 0x840, v0
	ds_write2_b32 v2, v14, v15 offset1:1
	v_add_u32_e32 v2, 0x848, v0
	ds_write2_b32 v2, v16, v17 offset1:1
	v_add_u32_e32 v2, 0xc60, v0
	ds_write2_b32 v2, v10, v11 offset1:1
	v_add_u32_e32 v2, 0xc68, v0
	ds_write2_b32 v2, v12, v13 offset1:1
	v_add_u32_e32 v2, 0x1080, v0
	ds_write2_b32 v2, v22, v23 offset1:1
	v_add_u32_e32 v2, 0x1088, v0
	ds_write2_b32 v2, v24, v25 offset1:1
	v_add_u32_e32 v2, 0x14a0, v0
	ds_write2_b32 v2, v18, v19 offset1:1
	v_add_u32_e32 v2, 0x14a8, v0
	ds_write2_b32 v2, v20, v21 offset1:1
	v_add_u32_e32 v2, 0x18c0, v0
	ds_write2_b32 v2, v30, v31 offset1:1
	v_add_u32_e32 v2, 0x18c8, v0
	ds_write2_b32 v2, v32, v33 offset1:1
	v_add_u32_e32 v2, 0x1ce0, v0
	v_add_u32_e32 v0, 0x1ce8, v0
	ds_write2_b32 v2, v26, v27 offset1:1
	ds_write2_b32 v0, v28, v29 offset1:1
	s_waitcnt lgkmcnt(0)
	v_lshl_add_u64 v[2:3], s[22:23], 1, v[60:61]
	v_cmp_gt_i32_e32 vcc, s26, v35
	s_and_saveexec_b64 s[4:5], vcc
	s_cbranch_execz .LBB0_484
	ds_read2_b32 v[4:5], v75 offset0:198 offset1:231
	ds_read2_b32 v[8:9], v75 offset0:132 offset1:165
	s_movk_i32 s21, 0x2c80
	s_waitcnt lgkmcnt(1)
	v_cvt_pk_bf16_f32 v7, v4, v5
	ds_read2_b32 v[4:5], v75 offset0:66 offset1:99
	s_waitcnt lgkmcnt(1)
	v_cvt_pk_bf16_f32 v6, v8, v9
	ds_read2_b32 v[8:9], v75 offset1:33
	s_waitcnt lgkmcnt(1)
	v_cvt_pk_bf16_f32 v5, v4, v5
	s_waitcnt lgkmcnt(0)
	v_cvt_pk_bf16_f32 v4, v8, v9
	v_or_b32_e32 v0, s20, v35
	v_mad_i64_i32 v[8:9], s[22:23], v0, s21, v[2:3]
	global_store_dwordx4 v[8:9], v[4:7], off
	s_or_b64 exec, exec, s[4:5]
	v_cmp_gt_i32_e32 vcc, s26, v69
	s_and_saveexec_b64 s[4:5], vcc
	s_cbranch_execnz .LBB0_485

; #define LAS __attribute__((address_space(3)))
; __device__ __forceinline__ unsigned pk2(float lo, float hi) { return f2bf(lo) | (f2bf(hi) << 16); }
; template <int MAPK>
; __device__ __forceinline__ void transpose_item(const float* W, int ldw, int k0, int n0, int ncnt, bf16* WT, int ldd, int dcol0, int moff, LAS float* scr, int lane, const float* gk) {
;     ...
;     const int c = lane & 7;
; #pragma unroll
;     for (int j = 0; j < 4; ++j) { const int n = (lane >> 3) + 8 * j; const LAS float* s = scr + (8 * c) * 33 + n;
;         v4u o; o.x = pk2(s[0 * 33], s[1 * 33]); o.y = pk2(s[2 * 33], s[3 * 33]); o.z = pk2(s[4 * 33], s[5 * 33]); o.w = pk2(s[6 * 33], s[7 * 33]);
;         const int sn = n0 + n - moff;
;         int drow;
;         if (MAPK == MAP_LIN) drow = sn; else if (MAPK == MAP_GATE) drow = 32 * (sn >> 4) + (sn & 15); else drow = 32 * (sn >> 4) + 16 + (sn & 15);
;         if (n < ncnt) *(v4u*)(WT + (size_t)drow * ldd + dcol0 + k0 + 8 * c) = o; }
.LBB0_483:
	ds_read2_b32 v[4:5], v75 offset0:214 offset1:247
	ds_read2_b32 v[8:9], v75 offset0:148 offset1:181
	s_movk_i32 s21, 0x2c80
	s_waitcnt lgkmcnt(1)
	v_cvt_pk_bf16_f32 v7, v4, v5
	ds_read2_b32 v[4:5], v75 offset0:82 offset1:115
	s_waitcnt lgkmcnt(1)
	v_cvt_pk_bf16_f32 v6, v8, v9
	ds_read2_b32 v[8:9], v75 offset0:16 offset1:49
	s_waitcnt lgkmcnt(1)
	v_cvt_pk_bf16_f32 v5, v4, v5
	s_waitcnt lgkmcnt(0)
	v_cvt_pk_bf16_f32 v4, v8, v9
	v_or_b32_e32 v0, s20, v71
	v_mad_i64_i32 v[8:9], s[22:23], v0, s21, v[2:3]
	global_store_dwordx4 v[8:9], v[4:7], off
	s_or_b64 exec, exec, s[4:5]
	v_cmp_gt_i32_e32 vcc, s26, v73
	s_and_saveexec_b64 s[4:5], vcc
	s_cbranch_execz .LBB0_23
	s_branch .LBB0_487

; #define LAS __attribute__((address_space(3)))
; __device__ __forceinline__ unsigned pk2(float lo, float hi) { return f2bf(lo) | (f2bf(hi) << 16); }
; template <int MAPK>
; __device__ __forceinline__ void transpose_item(const float* W, int ldw, int k0, int n0, int ncnt, bf16* WT, int ldd, int dcol0, int moff, LAS float* scr, int lane, const float* gk) {
;     ...
;     const int c = lane & 7;
; #pragma unroll
;     for (int j = 0; j < 4; ++j) { const int n = (lane >> 3) + 8 * j; const LAS float* s = scr + (8 * c) * 33 + n;
;         v4u o; o.x = pk2(s[0 * 33], s[1 * 33]); o.y = pk2(s[2 * 33], s[3 * 33]); o.z = pk2(s[4 * 33], s[5 * 33]); o.w = pk2(s[6 * 33], s[7 * 33]);
;         const int sn = n0 + n - moff;
;         int drow;
;         if (MAPK == MAP_LIN) drow = sn; else if (MAPK == MAP_GATE) drow = 32 * (sn >> 4) + (sn & 15); else drow = 32 * (sn >> 4) + 16 + (sn & 15);
;         if (n < ncnt) *(v4u*)(WT + (size_t)drow * ldd + dcol0 + k0 + 8 * c) = o; }
.LBB0_485:
	ds_read2_b32 v[4:5], v75 offset0:206 offset1:239
	ds_read2_b32 v[8:9], v75 offset0:140 offset1:173
	s_movk_i32 s21, 0x2c80
	s_waitcnt lgkmcnt(1)
	v_cvt_pk_bf16_f32 v7, v4, v5
	ds_read2_b32 v[4:5], v75 offset0:74 offset1:107
	s_waitcnt lgkmcnt(1)
	v_cvt_pk_bf16_f32 v6, v8, v9
	ds_read2_b32 v[8:9], v75 offset0:8 offset1:41
	s_waitcnt lgkmcnt(1)
	v_cvt_pk_bf16_f32 v5, v4, v5
	s_waitcnt lgkmcnt(0)
	v_cvt_pk_bf16_f32 v4, v8, v9
	v_or_b32_e32 v0, s20, v69
	v_mad_i64_i32 v[8:9], s[22:23], v0, s21, v[2:3]
	global_store_dwordx4 v[8:9], v[4:7], off
	s_or_b64 exec, exec, s[4:5]
	v_cmp_gt_i32_e32 vcc, s26, v71
	s_and_saveexec_b64 s[4:5], vcc
	s_cbranch_execnz .LBB0_483

; #define LAS __attribute__((address_space(3)))
; __device__ __forceinline__ unsigned pk2(float lo, float hi) { return f2bf(lo) | (f2bf(hi) << 16); }
; template <int MAPK>
; __device__ __forceinline__ void transpose_item(const float* W, int ldw, int k0, int n0, int ncnt, bf16* WT, int ldd, int dcol0, int moff, LAS float* scr, int lane, const float* gk) {
;     ...
;     const int c = lane & 7;
; #pragma unroll
;     for (int j = 0; j < 4; ++j) { const int n = (lane >> 3) + 8 * j; const LAS float* s = scr + (8 * c) * 33 + n;
;         v4u o; o.x = pk2(s[0 * 33], s[1 * 33]); o.y = pk2(s[2 * 33], s[3 * 33]); o.z = pk2(s[4 * 33], s[5 * 33]); o.w = pk2(s[6 * 33], s[7 * 33]);
;         const int sn = n0 + n - moff;
;         int drow;
;         if (MAPK == MAP_LIN) drow = sn; else if (MAPK == MAP_GATE) drow = 32 * (sn >> 4) + (sn & 15); else drow = 32 * (sn >> 4) + 16 + (sn & 15);
;         if (n < ncnt) *(v4u*)(WT + (size_t)drow * ldd + dcol0 + k0 + 8 * c) = o; }
.LBB0_487:
	ds_read2_b32 v[4:5], v75 offset0:222 offset1:255
	ds_read2_b32 v[8:9], v75 offset0:156 offset1:189
	s_waitcnt lgkmcnt(1)
	v_cvt_pk_bf16_f32 v7, v4, v5
	ds_read2_b32 v[4:5], v75 offset0:90 offset1:123
	s_waitcnt lgkmcnt(1)
	v_cvt_pk_bf16_f32 v6, v8, v9
	ds_read2_b32 v[8:9], v75 offset0:24 offset1:57
	s_waitcnt lgkmcnt(1)
	v_cvt_pk_bf16_f32 v5, v4, v5
	s_waitcnt lgkmcnt(0)
	v_cvt_pk_bf16_f32 v4, v8, v9
	v_or_b32_e32 v0, s20, v73
	s_movk_i32 s20, 0x2c80
	v_mad_i64_i32 v[2:3], s[20:21], v0, s20, v[2:3]
	global_store_dwordx4 v[2:3], v[4:7], off
	s_branch .LBB0_23
